# v043 + topk: second-half query fragments prefetched with the first half's (16 VGPRs freed by a 12-read MFMA window), copied at the second half
# baseline (speedup 1.0000x reference)
; #define LAS __attribute__((address_space(3)))
; __device__ __forceinline__ f32x4 mfma16(bf16x8 a, bf16x8 b, f32x4 c) { return __builtin_amdgcn_mfma_f32_16x16x32_bf16(a, b, c, 0, 0, 0); }
; __device__ __forceinline__ void topk_phase(LAS unsigned char* lds, const bf16_t* qp, const bf16_t* keys, const float* SU, const float* SV, int* sel_e, float* sel_g, float* sel_su, int G, int b) {
;     ...
;         unsigned T[2][16];
; #pragma unroll
;         for (int p = 0; p < 2; ++p) {
;             f32x4 acc[8];
; #pragma unroll
;             for (int mt = 0; mt < 8; ++mt) acc[mt] = (f32x4){0.f, 0.f, 0.f, 0.f};
;             bf16x8 bq[4];
; #pragma unroll
;             for (int ks = 0; ks < 4; ++ks) bq[ks] = *(const bf16x8*)(qp + (size_t)tok * D_ + h * 256 + p * 128 + ks * 32 + fq * 8);
;             const LAS bf16_t* kb = KL + p * 128 * 136;
; #pragma unroll
;             for (int mt = 0; mt < 8; ++mt)
; #pragma unroll
;                 for (int ks = 0; ks < 4; ++ks) { const bf16x8 a = *(const LAS bf16x8*)(kb + (mt * 16 + fr) * 136 + ks * 32 + fq * 8); acc[mt] = mfma16(a, bq[ks], acc[mt]); }
.LBB0_659:
	s_and_b32 s0, s52, 1
	s_lshl_b32 s1, s64, 8
	s_lshl_b32 s0, s0, 7
	s_or_b32 s0, s1, s0
	v_add_u32_e32 v94, s0, v85
	v_ashrrev_i32_e32 v95, 31, v94
	v_lshlrev_b64 v[34:35], 12, v[94:95]
	s_lshl_b32 s0, s56, 8
	v_lshl_add_u64 v[34:35], s[74:75], 0, v[34:35]
	s_ashr_i32 s1, s0, 31
	v_lshl_add_u64 v[34:35], s[0:1], 1, v[34:35]
	v_lshl_add_u64 v[96:97], v[34:35], 0, v[78:79]
	global_load_dwordx4 v[66:69], v[96:97], off
	global_load_dwordx4 v[62:65], v[96:97], off offset:64
	global_load_dwordx4 v[58:61], v[96:97], off offset:128
	global_load_dwordx4 v[54:57], v[96:97], off offset:192
	global_load_dwordx4 v[236:239], v[96:97], off offset:256
	global_load_dwordx4 v[244:247], v[96:97], off offset:320
	global_load_dwordx4 v[248:251], v[96:97], off offset:384
	global_load_dwordx4 v[252:255], v[96:97], off offset:448
	v_add_u32_e32 v138, v87, v89
	s_movk_i32 s0, 0xff
	ds_read_b128 v[174:177], v138 offset:32768
	ds_read_b128 v[178:181], v138 offset:37120
	ds_read_b128 v[182:185], v138 offset:41472
	ds_read_b128 v[186:189], v138 offset:45824
	ds_read_b128 v[190:193], v138 offset:50176
	ds_read_b128 v[194:197], v138 offset:54528
	ds_read_b128 v[198:201], v138 offset:58880
	ds_read_b128 v[216:219], v138 offset:32832
	ds_read_b128 v[220:223], v138 offset:37184
	ds_read_b128 v[224:227], v138 offset:41536
	ds_read_b128 v[228:231], v138 offset:45888
	ds_read_b128 v[232:235], v138 offset:50240
	s_waitcnt vmcnt(7) lgkmcnt(11)
	v_mfma_f32_16x16x32_bf16 v[46:49], v[174:177], v[66:69], 0
	ds_read_b128 v[174:177], v138 offset:54592
	s_waitcnt lgkmcnt(11)
	v_mfma_f32_16x16x32_bf16 v[34:37], v[178:181], v[66:69], 0
	ds_read_b128 v[178:181], v138 offset:58944
	s_waitcnt lgkmcnt(11)
	v_mfma_f32_16x16x32_bf16 v[38:41], v[182:185], v[66:69], 0
	ds_read_b128 v[182:185], v138 offset:32896
	s_waitcnt lgkmcnt(11)
	v_mfma_f32_16x16x32_bf16 v[42:45], v[186:189], v[66:69], 0
	ds_read_b128 v[186:189], v138 offset:37248
	s_waitcnt lgkmcnt(11)
	v_mfma_f32_16x16x32_bf16 v[70:73], v[190:193], v[66:69], 0
	ds_read_b128 v[190:193], v138 offset:41600
	s_waitcnt lgkmcnt(11)
	v_mfma_f32_16x16x32_bf16 v[50:53], v[194:197], v[66:69], 0
	ds_read_b128 v[194:197], v138 offset:45952
	s_waitcnt lgkmcnt(11)
	v_mfma_f32_16x16x32_bf16 v[74:77], v[198:201], v[66:69], 0
	ds_read_b128 v[198:201], v138 offset:50304
	s_waitcnt vmcnt(6) lgkmcnt(11)
	v_mfma_f32_16x16x32_bf16 v[46:49], v[216:219], v[62:65], v[46:49]
	ds_read_b128 v[216:219], v138 offset:54656
	s_waitcnt lgkmcnt(11)
	v_mfma_f32_16x16x32_bf16 v[34:37], v[220:223], v[62:65], v[34:37]
	ds_read_b128 v[220:223], v138 offset:59008
	s_waitcnt lgkmcnt(11)
	v_mfma_f32_16x16x32_bf16 v[38:41], v[224:227], v[62:65], v[38:41]
	ds_read_b128 v[224:227], v138 offset:32960
	s_waitcnt lgkmcnt(11)
	v_mfma_f32_16x16x32_bf16 v[42:45], v[228:231], v[62:65], v[42:45]
	ds_read_b128 v[228:231], v138 offset:37312
	s_waitcnt lgkmcnt(11)
	v_mfma_f32_16x16x32_bf16 v[70:73], v[232:235], v[62:65], v[70:73]
	ds_read_b128 v[232:235], v138 offset:41664
	s_waitcnt lgkmcnt(11)
	v_mfma_f32_16x16x32_bf16 v[50:53], v[174:177], v[62:65], v[50:53]
	ds_read_b128 v[174:177], v138 offset:46016
	s_waitcnt lgkmcnt(11)
	v_mfma_f32_16x16x32_bf16 v[74:77], v[178:181], v[62:65], v[74:77]
	ds_read_b128 v[178:181], v138 offset:50368
	s_waitcnt vmcnt(5) lgkmcnt(11)
	v_mfma_f32_16x16x32_bf16 v[46:49], v[182:185], v[58:61], v[46:49]
	ds_read_b128 v[182:185], v138 offset:54720
	s_waitcnt lgkmcnt(11)
	v_mfma_f32_16x16x32_bf16 v[34:37], v[186:189], v[58:61], v[34:37]
	ds_read_b128 v[186:189], v138 offset:59072
	s_waitcnt lgkmcnt(11)
	v_mfma_f32_16x16x32_bf16 v[38:41], v[190:193], v[58:61], v[38:41]
	ds_read_b128 v[190:193], v138 offset:63232
	s_waitcnt lgkmcnt(11)
	v_mfma_f32_16x16x32_bf16 v[42:45], v[194:197], v[58:61], v[42:45]
	ds_read_b128 v[194:197], v138 offset:63296
	s_waitcnt lgkmcnt(11)
	v_mfma_f32_16x16x32_bf16 v[70:73], v[198:201], v[58:61], v[70:73]
	ds_read_b128 v[198:201], v138 offset:63360
	s_waitcnt lgkmcnt(11)
	v_mfma_f32_16x16x32_bf16 v[50:53], v[216:219], v[58:61], v[50:53]
	ds_read_b128 v[216:219], v138 offset:63424
	s_waitcnt lgkmcnt(11)
	v_mfma_f32_16x16x32_bf16 v[74:77], v[220:223], v[58:61], v[74:77]
	s_waitcnt vmcnt(4) lgkmcnt(10)
	v_mfma_f32_16x16x32_bf16 v[46:49], v[224:227], v[54:57], v[46:49]
	s_waitcnt lgkmcnt(9)
	v_mfma_f32_16x16x32_bf16 v[34:37], v[228:231], v[54:57], v[34:37]
	s_waitcnt lgkmcnt(8)
	v_mfma_f32_16x16x32_bf16 v[38:41], v[232:235], v[54:57], v[38:41]
	s_waitcnt lgkmcnt(7)
	v_mfma_f32_16x16x32_bf16 v[42:45], v[174:177], v[54:57], v[42:45]
	s_waitcnt lgkmcnt(6)
	v_mfma_f32_16x16x32_bf16 v[70:73], v[178:181], v[54:57], v[70:73]
	s_waitcnt lgkmcnt(5)
	v_mfma_f32_16x16x32_bf16 v[50:53], v[182:185], v[54:57], v[50:53]
	s_waitcnt lgkmcnt(4)
	v_mfma_f32_16x16x32_bf16 v[74:77], v[186:189], v[54:57], v[74:77]
	s_waitcnt lgkmcnt(3)
	v_mfma_f32_16x16x32_bf16 v[66:69], v[190:193], v[66:69], 0
	s_waitcnt lgkmcnt(2)
	v_mfma_f32_16x16x32_bf16 v[62:65], v[194:197], v[62:65], v[66:69]
	s_waitcnt lgkmcnt(1)
	v_mfma_f32_16x16x32_bf16 v[58:61], v[198:201], v[58:61], v[62:65]
	s_waitcnt lgkmcnt(0)
; __device__ __forceinline__ unsigned mono(float f) { const unsigned u = __float_as_uint(f); return (u & 0x80000000u) ? ~u : (u ^ 0x80000000u); }
; __device__ __forceinline__ void topk_phase(LAS unsigned char* lds, const bf16_t* qp, const bf16_t* keys, const float* SU, const float* SV, int* sel_e, float* sel_g, float* sel_su, int G, int b) {
;     ...
;             unsigned lo16[16];
; #pragma unroll
;             for (int mt = 0; mt < 4; ++mt)
; #pragma unroll
;                 for (int r = 0; r < 4; ++r) {
;                     T[p][mt * 4 + r] = (mono(acc[mt][r]) & ~127u) | (unsigned)(127 - (mt * 16 + fq * 4 + r));
;                     lo16[mt * 4 + r] = (mono(acc[mt + 4][r]) & ~127u) | (unsigned)(127 - ((mt + 4) * 16 + fq * 4 + r));
;                 }
;             SN_SORT16(T[p]); SN_SORT16(lo16);
	v_mfma_f32_16x16x32_bf16 v[54:57], v[216:219], v[54:57], v[58:61]
	s_nop 2
	v_ashrrev_i32_e32 v58, 31, v46
	v_bitop3_b32 v46, v46, v58, v132 bitop3:0x1e
	v_and_or_b32 v46, v46, s53, v98
	v_ashrrev_i32_e32 v58, 31, v70
	v_bitop3_b32 v58, v70, v58, v132 bitop3:0x1e
	v_and_or_b32 v58, v58, s53, v99
	v_ashrrev_i32_e32 v59, 31, v47
	v_bitop3_b32 v47, v47, v59, v132 bitop3:0x1e
	v_and_or_b32 v47, v47, s53, v100
	v_ashrrev_i32_e32 v59, 31, v71
	v_bitop3_b32 v59, v71, v59, v132 bitop3:0x1e
	v_and_or_b32 v59, v59, s53, v101
	v_ashrrev_i32_e32 v60, 31, v48
	v_bitop3_b32 v48, v48, v60, v132 bitop3:0x1e
	v_and_or_b32 v48, v48, s53, v102
	v_ashrrev_i32_e32 v60, 31, v72
	v_bitop3_b32 v60, v72, v60, v132 bitop3:0x1e
	v_and_or_b32 v60, v60, s53, v103
	v_ashrrev_i32_e32 v61, 31, v49
	v_bitop3_b32 v49, v49, v61, v132 bitop3:0x1e
	v_and_or_b32 v49, v49, s53, v104
	v_ashrrev_i32_e32 v61, 31, v73
	v_bitop3_b32 v61, v73, v61, v132 bitop3:0x1e
	v_and_or_b32 v61, v61, s53, v105
	v_ashrrev_i32_e32 v62, 31, v34
	v_bitop3_b32 v34, v34, v62, v132 bitop3:0x1e
	v_and_or_b32 v34, v34, s53, v106
	v_ashrrev_i32_e32 v62, 31, v50
	v_bitop3_b32 v50, v50, v62, v132 bitop3:0x1e
	v_and_or_b32 v50, v50, s53, v107
	v_ashrrev_i32_e32 v62, 31, v35
	v_bitop3_b32 v35, v35, v62, v132 bitop3:0x1e
	v_and_or_b32 v35, v35, s53, v108
	v_ashrrev_i32_e32 v62, 31, v51
	v_bitop3_b32 v51, v51, v62, v132 bitop3:0x1e
	v_and_or_b32 v51, v51, s53, v109
	v_ashrrev_i32_e32 v62, 31, v36
	v_bitop3_b32 v36, v36, v62, v132 bitop3:0x1e
	v_and_or_b32 v36, v36, s53, v110
	v_ashrrev_i32_e32 v62, 31, v52
	v_bitop3_b32 v52, v52, v62, v132 bitop3:0x1e
	v_and_or_b32 v52, v52, s53, v111
	v_ashrrev_i32_e32 v62, 31, v37
	v_bitop3_b32 v37, v37, v62, v132 bitop3:0x1e
	v_and_or_b32 v37, v37, s53, v112
	v_ashrrev_i32_e32 v62, 31, v53
	v_bitop3_b32 v53, v53, v62, v132 bitop3:0x1e
	v_and_or_b32 v53, v53, s53, v113
	v_ashrrev_i32_e32 v62, 31, v38
	v_bitop3_b32 v38, v38, v62, v132 bitop3:0x1e
	v_and_or_b32 v38, v38, s53, v114
	v_ashrrev_i32_e32 v62, 31, v74
	v_bitop3_b32 v62, v74, v62, v132 bitop3:0x1e
	v_max_u32_e32 v74, v58, v59
	v_ashrrev_i32_e32 v63, 31, v39
	v_cmp_lt_i32_e32 vcc, -1, v75
	v_bitop3_b32 v39, v39, v63, v132 bitop3:0x1e
	v_min_u32_e32 v58, v58, v59
	v_cndmask_b32_e32 v63, -1, v132, vcc
	v_max_u32_e32 v59, v60, v61
	v_min_u32_e32 v60, v60, v61
	v_ashrrev_i32_e32 v64, 31, v40
	v_cmp_lt_i32_e32 vcc, -1, v76
	v_bitop3_b32 v40, v40, v64, v132 bitop3:0x1e
	v_max_u32_e32 v61, v74, v59
	v_cndmask_b32_e32 v64, -1, v132, vcc
	v_min_u32_e32 v59, v74, v59
	v_max_u32_e32 v74, v58, v60
	v_ashrrev_i32_e32 v65, 31, v41
	v_cmp_lt_i32_e32 vcc, -1, v77
	v_bitop3_b32 v41, v41, v65, v132 bitop3:0x1e
	v_min_u32_e32 v58, v58, v60
	v_cndmask_b32_e32 v65, -1, v132, vcc
	v_max_u32_e32 v60, v74, v59
	v_min_u32_e32 v59, v74, v59
	v_ashrrev_i32_e32 v66, 31, v42
	v_bitop3_b32 v42, v42, v66, v132 bitop3:0x1e
	v_max_u32_e32 v74, v50, v51
	v_ashrrev_i32_e32 v66, 31, v54
	v_bitop3_b32 v54, v54, v66, v132 bitop3:0x1e
	v_min_u32_e32 v50, v50, v51
	v_ashrrev_i32_e32 v66, 31, v43
	v_bitop3_b32 v43, v43, v66, v132 bitop3:0x1e
	v_max_u32_e32 v51, v52, v53
	v_ashrrev_i32_e32 v66, 31, v55
	v_bitop3_b32 v55, v55, v66, v132 bitop3:0x1e
	v_min_u32_e32 v52, v52, v53
	v_ashrrev_i32_e32 v66, 31, v44
	v_bitop3_b32 v44, v44, v66, v132 bitop3:0x1e
	v_max_u32_e32 v53, v74, v51
	v_ashrrev_i32_e32 v66, 31, v56
	v_bitop3_b32 v56, v56, v66, v132 bitop3:0x1e
	v_min_u32_e32 v51, v74, v51
	v_ashrrev_i32_e32 v66, 31, v45
	v_cmp_lt_i32_e32 vcc, -1, v57
	v_bitop3_b32 v45, v45, v66, v132 bitop3:0x1e
	v_max_u32_e32 v74, v50, v52
	v_cndmask_b32_e32 v66, -1, v132, vcc
	v_xor_b32_e32 v57, v66, v57
	v_max_u32_e32 v66, v46, v47
	v_min_u32_e32 v46, v46, v47
	v_max_u32_e32 v47, v48, v49
	v_min_u32_e32 v48, v48, v49
	v_max_u32_e32 v49, v66, v47
	v_min_u32_e32 v47, v66, v47
	v_max_u32_e32 v66, v46, v48
	v_min_u32_e32 v46, v46, v48
	v_max_u32_e32 v48, v66, v47
	v_min_u32_e32 v47, v66, v47
	v_max_u32_e32 v66, v34, v35
	v_min_u32_e32 v34, v34, v35
	v_max_u32_e32 v35, v36, v37
	v_min_u32_e32 v36, v36, v37
	v_max_u32_e32 v37, v66, v35
	v_min_u32_e32 v35, v66, v35
	v_max_u32_e32 v66, v34, v36
	v_min_u32_e32 v34, v34, v36
	v_max_u32_e32 v36, v66, v35
	v_min_u32_e32 v35, v66, v35
	v_min_u32_e32 v50, v50, v52
	v_max_u32_e32 v52, v74, v51
	v_min_u32_e32 v51, v74, v51
	v_max_u32_e32 v66, v49, v37
	v_min_u32_e32 v37, v49, v37
	v_max_u32_e32 v49, v47, v35
	v_max_u32_e32 v74, v61, v53
	v_min_u32_e32 v53, v61, v53
	v_max_u32_e32 v61, v59, v51
	v_xor_b32_e32 v63, v63, v75
	v_xor_b32_e32 v64, v64, v76
	v_xor_b32_e32 v65, v65, v77
	v_min_u32_e32 v35, v47, v35
	v_max_u32_e32 v47, v49, v37
	v_min_u32_e32 v37, v49, v37
	v_max_u32_e32 v49, v48, v36
	v_min_u32_e32 v36, v48, v36
	v_max_u32_e32 v48, v46, v34
	v_min_u32_e32 v51, v59, v51
	v_max_u32_e32 v59, v61, v53
	v_min_u32_e32 v53, v61, v53
	v_max_u32_e32 v61, v60, v52
	v_min_u32_e32 v52, v60, v52
	v_max_u32_e32 v60, v58, v50
	v_and_or_b32 v62, v62, s53, v115
	v_and_or_b32 v39, v39, s53, v116
	v_and_or_b32 v63, v63, s53, v117
	v_and_or_b32 v40, v40, s53, v118
	v_and_or_b32 v64, v64, s53, v119
	v_and_or_b32 v41, v41, s53, v120
	v_and_or_b32 v65, v65, s53, v121
	v_min_u32_e32 v34, v46, v34
	v_max_u32_e32 v46, v48, v36
	v_min_u32_e32 v36, v48, v36
	v_min_u32_e32 v50, v58, v50
	v_max_u32_e32 v58, v60, v52
	v_min_u32_e32 v52, v60, v52
	v_max_u32_e32 v48, v49, v47
	v_min_u32_e32 v47, v49, v47
	v_max_u32_e32 v49, v46, v37
	v_min_u32_e32 v37, v46, v37
	v_max_u32_e32 v46, v36, v35
	v_min_u32_e32 v35, v36, v35
	v_max_u32_e32 v36, v38, v39
	v_min_u32_e32 v38, v38, v39
	v_max_u32_e32 v39, v40, v41
	v_min_u32_e32 v40, v40, v41
	v_max_u32_e32 v60, v61, v59
; __device__ __forceinline__ void topk_phase(LAS unsigned char* lds, const bf16_t* qp, const bf16_t* keys, const float* SU, const float* SV, int* sel_e, float* sel_g, float* sel_su, int G, int b) {
;     ...
;             SN_SORT16(T[p]); SN_SORT16(lo16);
; #pragma unroll
;             for (int i = 0; i < 16; ++i) T[p][i] = umax_(T[p][i], lo16[15 - i]);
;             SN_BITONIC16(T[p]);
	v_min_u32_e32 v59, v61, v59
	v_max_u32_e32 v61, v58, v53
	v_min_u32_e32 v53, v58, v53
	v_max_u32_e32 v58, v52, v51
	v_min_u32_e32 v51, v52, v51
	v_max_u32_e32 v52, v62, v63
	v_min_u32_e32 v62, v62, v63
	v_max_u32_e32 v63, v64, v65
	v_min_u32_e32 v64, v64, v65
	v_and_or_b32 v42, v42, s53, v122
	v_and_or_b32 v54, v54, s53, v123
	v_and_or_b32 v43, v43, s53, v124
	v_and_or_b32 v55, v55, s53, v125
	v_and_or_b32 v44, v44, s53, v126
	v_and_or_b32 v56, v56, s53, v127
	v_and_or_b32 v45, v45, s53, v128
	v_and_or_b32 v57, v57, s53, v129
	v_max_u32_e32 v41, v36, v39
	v_min_u32_e32 v36, v36, v39
	v_max_u32_e32 v39, v38, v40
	v_max_u32_e32 v65, v52, v63
	v_min_u32_e32 v52, v52, v63
	v_max_u32_e32 v63, v62, v64
	v_min_u32_e32 v38, v38, v40
	v_max_u32_e32 v40, v39, v36
	v_min_u32_e32 v36, v39, v36
	v_max_u32_e32 v39, v42, v43
	v_min_u32_e32 v42, v42, v43
	v_max_u32_e32 v43, v44, v45
	v_min_u32_e32 v44, v44, v45
	v_min_u32_e32 v62, v62, v64
	v_max_u32_e32 v64, v63, v52
	v_min_u32_e32 v52, v63, v52
	v_max_u32_e32 v63, v54, v55
	v_min_u32_e32 v54, v54, v55
	v_max_u32_e32 v55, v56, v57
	v_min_u32_e32 v56, v56, v57
	v_max_u32_e32 v45, v39, v43
	v_min_u32_e32 v39, v39, v43
	v_max_u32_e32 v43, v42, v44
	v_max_u32_e32 v57, v63, v55
	v_min_u32_e32 v55, v63, v55
	v_max_u32_e32 v63, v54, v56
	v_min_u32_e32 v42, v42, v44
	v_max_u32_e32 v44, v43, v39
	v_min_u32_e32 v39, v43, v39
	v_min_u32_e32 v54, v54, v56
	v_max_u32_e32 v56, v63, v55
	v_min_u32_e32 v55, v63, v55
	v_max_u32_e32 v43, v41, v45
	v_min_u32_e32 v41, v41, v45
	v_max_u32_e32 v45, v36, v39
	v_max_u32_e32 v63, v65, v57
	v_min_u32_e32 v57, v65, v57
	v_max_u32_e32 v65, v52, v55
	v_min_u32_e32 v36, v36, v39
	v_max_u32_e32 v39, v45, v41
	v_min_u32_e32 v41, v45, v41
	v_max_u32_e32 v45, v40, v44
	v_min_u32_e32 v40, v40, v44
	v_max_u32_e32 v44, v38, v42
	v_min_u32_e32 v52, v52, v55
	v_max_u32_e32 v55, v65, v57
	v_min_u32_e32 v57, v65, v57
	v_max_u32_e32 v65, v64, v56
	v_min_u32_e32 v56, v64, v56
	v_max_u32_e32 v64, v62, v54
	v_min_u32_e32 v38, v38, v42
	v_max_u32_e32 v42, v44, v40
	v_min_u32_e32 v54, v62, v54
	v_max_u32_e32 v62, v64, v56
	v_min_u32_e32 v40, v44, v40
	v_max_u32_e32 v44, v45, v39
	v_min_u32_e32 v39, v45, v39
	v_max_u32_e32 v45, v42, v41
	v_min_u32_e32 v41, v42, v41
	v_min_u32_e32 v56, v64, v56
	v_max_u32_e32 v64, v65, v55
	v_min_u32_e32 v55, v65, v55
	v_max_u32_e32 v65, v62, v57
	v_min_u32_e32 v57, v62, v57
	v_max_u32_e32 v42, v40, v36
	v_min_u32_e32 v36, v40, v36
	v_min_u32_e32 v40, v66, v43
	v_max_u32_e32 v67, v37, v41
	v_max_u32_e32 v62, v56, v52
	v_min_u32_e32 v52, v56, v52
	v_min_u32_e32 v56, v74, v63
	v_max_u32_e32 v75, v53, v57
	v_min_u32_e32 v37, v37, v41
	v_max_u32_e32 v41, v67, v40
	v_min_u32_e32 v40, v67, v40
	v_max_u32_e32 v67, v47, v39
	v_min_u32_e32 v39, v47, v39
	v_max_u32_e32 v47, v35, v36
	v_min_u32_e32 v53, v53, v57
	v_max_u32_e32 v57, v75, v56
	v_min_u32_e32 v56, v75, v56
	v_max_u32_e32 v75, v59, v55
	v_min_u32_e32 v55, v59, v55
	v_max_u32_e32 v59, v51, v52
	v_min_u32_e32 v35, v35, v36
	v_max_u32_e32 v36, v47, v39
	v_min_u32_e32 v39, v47, v39
	v_min_u32_e32 v51, v51, v52
	v_max_u32_e32 v52, v59, v55
	v_min_u32_e32 v55, v59, v55
	v_max_u32_e32 v47, v67, v41
	v_min_u32_e32 v41, v67, v41
	v_max_u32_e32 v67, v36, v40
	v_min_u32_e32 v36, v36, v40
	v_max_u32_e32 v40, v39, v37
	v_min_u32_e32 v37, v39, v37
	v_max_u32_e32 v39, v48, v44
	v_min_u32_e32 v44, v48, v44
	v_max_u32_e32 v48, v46, v42
	v_max_u32_e32 v59, v75, v57
	v_min_u32_e32 v57, v75, v57
	v_max_u32_e32 v75, v52, v56
	v_min_u32_e32 v52, v52, v56
	v_max_u32_e32 v56, v55, v53
	v_min_u32_e32 v53, v55, v53
	v_max_u32_e32 v55, v60, v64
	v_min_u32_e32 v60, v60, v64
	v_max_u32_e32 v64, v58, v62
	v_min_u32_e32 v42, v46, v42
	v_max_u32_e32 v46, v48, v44
	v_min_u32_e32 v44, v48, v44
	v_max_u32_e32 v48, v49, v45
	v_min_u32_e32 v45, v49, v45
	v_max_u32_e32 v49, v34, v38
	v_min_u32_e32 v58, v58, v62
	v_max_u32_e32 v62, v64, v60
	v_min_u32_e32 v60, v64, v60
	v_max_u32_e32 v64, v61, v65
	v_min_u32_e32 v61, v61, v65
	v_max_u32_e32 v65, v50, v54
	v_min_u32_e32 v34, v34, v38
	v_max_u32_e32 v38, v49, v45
	v_min_u32_e32 v45, v49, v45
	v_min_u32_e32 v50, v50, v54
	v_max_u32_e32 v54, v65, v61
	v_min_u32_e32 v61, v65, v61
	v_max_u32_e32 v49, v48, v46
	v_min_u32_e32 v46, v48, v46
	v_max_u32_e32 v48, v38, v44
	v_min_u32_e32 v38, v38, v44
	v_max_u32_e32 v44, v45, v42
	v_min_u32_e32 v42, v45, v42
	v_max_u32_e32 v65, v64, v62
	v_min_u32_e32 v62, v64, v62
	v_max_u32_e32 v64, v54, v60
	v_min_u32_e32 v54, v54, v60
	v_max_u32_e32 v60, v61, v58
	v_min_u32_e32 v58, v61, v58
	v_min_u32_e32 v45, v39, v47
	v_min_u32_e32 v68, v49, v41
	v_min_u32_e32 v69, v46, v67
	v_min_u32_e32 v70, v48, v36
	v_min_u32_e32 v71, v38, v40
	v_min_u32_e32 v72, v44, v37
	v_min_u32_e32 v73, v42, v35
	v_min_u32_e32 v61, v55, v59
	v_min_u32_e32 v76, v65, v57
	v_min_u32_e32 v77, v62, v75
	v_min_u32_e32 v134, v64, v52
	v_min_u32_e32 v135, v54, v56
	v_min_u32_e32 v136, v60, v53
	v_min_u32_e32 v137, v58, v51
	v_max3_u32 v43, v66, v43, v50
	v_max3_u32 v39, v39, v47, v137
	v_max3_u32 v45, v45, v58, v51
	v_max3_u32 v41, v49, v41, v136
	v_max3_u32 v47, v68, v60, v53
	v_max3_u32 v46, v46, v67, v135
	v_max3_u32 v49, v69, v54, v56
	v_max3_u32 v36, v48, v36, v134
	v_max3_u32 v48, v70, v64, v52
	v_max3_u32 v38, v38, v40, v77
	v_max3_u32 v40, v71, v62, v75
	v_max3_u32 v37, v44, v37, v76
	v_max3_u32 v44, v72, v65, v57
	v_max3_u32 v35, v42, v35, v61
	v_max3_u32 v42, v73, v55, v59
	v_max3_u32 v34, v34, v74, v63
	v_max_u32_e32 v50, v43, v48
	v_min_u32_e32 v43, v43, v48
	v_max_u32_e32 v48, v39, v38
	v_min_u32_e32 v38, v39, v38
	v_max_u32_e32 v39, v45, v40
	v_min_u32_e32 v40, v45, v40
	v_max_u32_e32 v45, v41, v37
; #define LAS __attribute__((address_space(3)))
; __device__ __forceinline__ f32x4 mfma16(bf16x8 a, bf16x8 b, f32x4 c) { return __builtin_amdgcn_mfma_f32_16x16x32_bf16(a, b, c, 0, 0, 0); }
; __device__ __forceinline__ void topk_phase(LAS unsigned char* lds, const bf16_t* qp, const bf16_t* keys, const float* SU, const float* SV, int* sel_e, float* sel_g, float* sel_su, int G, int b) {
;     ...
;             for (int ks = 0; ks < 4; ++ks) bq[ks] = *(const bf16x8*)(qp + (size_t)tok * D_ + h * 256 + p * 128 + ks * 32 + fq * 8);
;             const LAS bf16_t* kb = KL + p * 128 * 136;
; #pragma unroll
;             for (int mt = 0; mt < 8; ++mt)
; #pragma unroll
;                 for (int ks = 0; ks < 4; ++ks) { const bf16x8 a = *(const LAS bf16x8*)(kb + (mt * 16 + fr) * 136 + ks * 32 + fq * 8); acc[mt] = mfma16(a, bq[ks], acc[mt]); }
	v_min_u32_e32 v37, v41, v37
	v_max_u32_e32 v41, v47, v44
	v_min_u32_e32 v44, v47, v44
	v_max_u32_e32 v47, v46, v35
	v_min_u32_e32 v35, v46, v35
	v_max_u32_e32 v46, v49, v42
	v_min_u32_e32 v42, v49, v42
	v_max_u32_e32 v49, v36, v34
	v_min_u32_e32 v34, v36, v34
	v_max_u32_e32 v36, v50, v41
	v_min_u32_e32 v41, v50, v41
	v_max_u32_e32 v50, v48, v47
	v_min_u32_e32 v47, v48, v47
	v_max_u32_e32 v48, v39, v46
	v_min_u32_e32 v39, v39, v46
	v_max_u32_e32 v46, v45, v49
	v_min_u32_e32 v45, v45, v49
	v_max_u32_e32 v49, v43, v44
	v_min_u32_e32 v43, v43, v44
	v_max_u32_e32 v44, v38, v35
	v_min_u32_e32 v35, v38, v35
	v_max_u32_e32 v38, v40, v42
	v_min_u32_e32 v40, v40, v42
	v_max_u32_e32 v42, v37, v34
	v_min_u32_e32 v34, v37, v34
	v_max_u32_e32 v37, v36, v48
	v_min_u32_e32 v36, v36, v48
	v_max_u32_e32 v48, v50, v46
	v_min_u32_e32 v46, v50, v46
	v_max_u32_e32 v50, v41, v39
	v_min_u32_e32 v39, v41, v39
	v_max_u32_e32 v41, v47, v45
	v_min_u32_e32 v45, v47, v45
	v_max_u32_e32 v47, v49, v38
	v_min_u32_e32 v38, v49, v38
	v_max_u32_e32 v49, v44, v42
	v_min_u32_e32 v42, v44, v42
	v_max_u32_e32 v44, v43, v40
	v_min_u32_e32 v40, v43, v40
	v_max_u32_e32 v43, v35, v34
	v_min_u32_e32 v34, v35, v34
	v_max_u32_e32 v35, v37, v48
	v_min_u32_e32 v37, v37, v48
	v_max_u32_e32 v48, v36, v46
	v_min_u32_e32 v36, v36, v46
	v_max_u32_e32 v46, v50, v41
	v_min_u32_e32 v41, v50, v41
	v_max_u32_e32 v50, v39, v45
	v_min_u32_e32 v39, v39, v45
	v_max_u32_e32 v45, v47, v49
	v_min_u32_e32 v47, v47, v49
	v_max_u32_e32 v49, v38, v42
	v_min_u32_e32 v38, v38, v42
	v_max_u32_e32 v42, v44, v43
	v_min_u32_e32 v43, v44, v43
	v_max_u32_e32 v44, v40, v34
	v_min_u32_e32 v34, v40, v34
	v_mov_b32_e32 v40, v35
	v_mov_b32_e32 v51, v37
	v_mov_b32_e32 v52, v48
	v_mov_b32_e32 v53, v36
	v_mov_b32_e32 v54, v46
	v_mov_b32_e32 v55, v41
	v_mov_b32_e32 v56, v50
	v_mov_b32_e32 v57, v39
	v_mov_b32_e32 v58, v45
	v_mov_b32_e32 v59, v47
	v_mov_b32_e32 v60, v49
	v_mov_b32_e32 v61, v38
	v_mov_b32_e32 v62, v42
	v_mov_b32_e32 v63, v43
	v_mov_b32_e32 v64, v44
	v_mov_b32_e32 v65, v34
	v_permlane16_swap_b32_e32 v35, v40
	v_permlane16_swap_b32_e32 v37, v51
	v_permlane16_swap_b32_e32 v48, v52
	v_permlane16_swap_b32_e32 v36, v53
	v_permlane16_swap_b32_e32 v46, v54
	v_permlane16_swap_b32_e32 v41, v55
	v_permlane16_swap_b32_e32 v50, v56
	v_permlane16_swap_b32_e32 v39, v57
	v_permlane16_swap_b32_e32 v45, v58
	v_permlane16_swap_b32_e32 v47, v59
	v_permlane16_swap_b32_e32 v49, v60
	v_permlane16_swap_b32_e32 v38, v61
	v_permlane16_swap_b32_e32 v42, v62
	v_permlane16_swap_b32_e32 v43, v63
	v_permlane16_swap_b32_e32 v44, v64
	v_permlane16_swap_b32_e32 v34, v65
	v_max_u32_e32 v35, v35, v65
	v_max_u32_e32 v37, v37, v64
	v_max_u32_e32 v48, v48, v63
	v_max_u32_e32 v36, v36, v62
	v_max_u32_e32 v46, v46, v61
	v_max_u32_e32 v41, v41, v60
	v_max_u32_e32 v50, v50, v59
	v_max_u32_e32 v39, v39, v58
	v_max_u32_e32 v45, v45, v57
	v_max_u32_e32 v47, v47, v56
	v_max_u32_e32 v49, v49, v55
	v_max_u32_e32 v38, v38, v54
	v_max_u32_e32 v42, v42, v53
	v_max_u32_e32 v43, v43, v52
	v_max_u32_e32 v44, v44, v51
	v_max_u32_e32 v34, v34, v40
	v_max_u32_e32 v40, v35, v45
	v_min_u32_e32 v35, v35, v45
	v_max_u32_e32 v45, v37, v47
	v_min_u32_e32 v37, v37, v47
	v_max_u32_e32 v47, v48, v49
	v_min_u32_e32 v48, v48, v49
	v_max_u32_e32 v49, v36, v38
	v_min_u32_e32 v36, v36, v38
	v_max_u32_e32 v38, v46, v42
	v_min_u32_e32 v42, v46, v42
	v_max_u32_e32 v46, v41, v43
	v_min_u32_e32 v41, v41, v43
	v_max_u32_e32 v43, v50, v44
	v_min_u32_e32 v44, v50, v44
	v_max_u32_e32 v50, v39, v34
	v_min_u32_e32 v34, v39, v34
	v_max_u32_e32 v39, v40, v38
	v_min_u32_e32 v38, v40, v38
	v_max_u32_e32 v40, v45, v46
	v_min_u32_e32 v45, v45, v46
	v_max_u32_e32 v46, v47, v43
	v_min_u32_e32 v43, v47, v43
	v_max_u32_e32 v47, v49, v50
	v_min_u32_e32 v49, v49, v50
	v_max_u32_e32 v50, v35, v42
	v_min_u32_e32 v35, v35, v42
	v_max_u32_e32 v42, v37, v41
	v_min_u32_e32 v37, v37, v41
	v_max_u32_e32 v41, v48, v44
	v_min_u32_e32 v44, v48, v44
	v_max_u32_e32 v48, v36, v34
	v_min_u32_e32 v34, v36, v34
	v_max_u32_e32 v36, v39, v46
	v_min_u32_e32 v39, v39, v46
	v_max_u32_e32 v46, v40, v47
	v_min_u32_e32 v40, v40, v47
	v_max_u32_e32 v47, v38, v43
	v_min_u32_e32 v38, v38, v43
	v_max_u32_e32 v43, v45, v49
	v_min_u32_e32 v45, v45, v49
	v_max_u32_e32 v49, v50, v41
	v_min_u32_e32 v41, v50, v41
	v_max_u32_e32 v50, v42, v48
	v_min_u32_e32 v42, v42, v48
	v_max_u32_e32 v48, v35, v44
	v_min_u32_e32 v35, v35, v44
	v_max_u32_e32 v44, v37, v34
	v_min_u32_e32 v34, v37, v34
	v_max_u32_e32 v70, v36, v46
	v_min_u32_e32 v71, v36, v46
	v_max_u32_e32 v72, v39, v40
	v_min_u32_e32 v73, v39, v40
	v_max_u32_e32 v74, v47, v43
	v_min_u32_e32 v75, v47, v43
	v_max_u32_e32 v76, v38, v45
	v_min_u32_e32 v77, v38, v45
	v_max_u32_e32 v134, v49, v50
	v_min_u32_e32 v135, v49, v50
	v_max_u32_e32 v136, v41, v42
	v_min_u32_e32 v137, v41, v42
	v_max_u32_e32 v138, v48, v44
	v_min_u32_e32 v139, v48, v44
	v_max_u32_e32 v140, v35, v34
	v_min_u32_e32 v141, v35, v34
	s_waitcnt vmcnt(0)
	v_mov_b64_e32 v[46:47], v[236:237]
	v_mov_b64_e32 v[48:49], v[238:239]
	v_mov_b64_e32 v[42:43], v[244:245]
	v_mov_b64_e32 v[44:45], v[246:247]
	v_mov_b64_e32 v[38:39], v[248:249]
	v_mov_b64_e32 v[40:41], v[250:251]
	v_mov_b64_e32 v[34:35], v[252:253]
	v_mov_b64_e32 v[36:37], v[254:255]
	ds_read_b128 v[50:53], v131 offset:34816
	ds_read_b128 v[54:57], v131 offset:34880
	s_waitcnt vmcnt(3) lgkmcnt(1)
	v_mfma_f32_16x16x32_bf16 v[50:53], v[50:53], v[46:49], 0
	ds_read_b128 v[58:61], v131 offset:39232
	ds_read_b128 v[62:65], v131 offset:43584
	ds_read_b128 v[66:69], v131 offset:47936
	s_waitcnt vmcnt(2) lgkmcnt(3)
; #define LAS __attribute__((address_space(3)))
; __device__ __forceinline__ f32x4 mfma16(bf16x8 a, bf16x8 b, f32x4 c) { return __builtin_amdgcn_mfma_f32_16x16x32_bf16(a, b, c, 0, 0, 0); }
; __device__ __forceinline__ void topk_phase(LAS unsigned char* lds, const bf16_t* qp, const bf16_t* keys, const float* SU, const float* SV, int* sel_e, float* sel_g, float* sel_su, int G, int b) {
;     ...
;             for (int ks = 0; ks < 4; ++ks) bq[ks] = *(const bf16x8*)(qp + (size_t)tok * D_ + h * 256 + p * 128 + ks * 32 + fq * 8);
;             const LAS bf16_t* kb = KL + p * 128 * 136;
; #pragma unroll
;             for (int mt = 0; mt < 8; ++mt)
; #pragma unroll
;                 for (int ks = 0; ks < 4; ++ks) { const bf16x8 a = *(const LAS bf16x8*)(kb + (mt * 16 + fr) * 136 + ks * 32 + fq * 8); acc[mt] = mfma16(a, bq[ks], acc[mt]); }
	v_mfma_f32_16x16x32_bf16 v[50:53], v[54:57], v[42:45], v[50:53]
	ds_read_b128 v[54:57], v131 offset:34944
	ds_read_b128 v[158:161], v131 offset:52288
	ds_read_b128 v[162:165], v131 offset:56640
	s_waitcnt vmcnt(1) lgkmcnt(2)
	v_mfma_f32_16x16x32_bf16 v[50:53], v[54:57], v[38:41], v[50:53]
	ds_read_b128 v[54:57], v131 offset:35008
	ds_read_b128 v[166:169], v131 offset:60992
	v_mov_b32_e32 v142, v70
	s_waitcnt vmcnt(0) lgkmcnt(1)
	v_mfma_f32_16x16x32_bf16 v[50:53], v[54:57], v[34:37], v[50:53]
	ds_read_b128 v[54:57], v131 offset:39168
	v_mov_b32_e32 v143, v71
	v_mov_b32_e32 v144, v72
	s_waitcnt lgkmcnt(0)
	v_mfma_f32_16x16x32_bf16 v[54:57], v[54:57], v[46:49], 0
	s_nop 2
	v_mov_b32_e32 v145, v73
	v_mov_b32_e32 v146, v74
	v_mfma_f32_16x16x32_bf16 v[54:57], v[58:61], v[42:45], v[54:57]
	ds_read_b128 v[58:61], v131 offset:39296
	v_mov_b32_e32 v147, v75
	v_mov_b32_e32 v148, v76
	s_waitcnt lgkmcnt(0)
	v_mfma_f32_16x16x32_bf16 v[54:57], v[58:61], v[38:41], v[54:57]
	ds_read_b128 v[58:61], v131 offset:39360
	v_mov_b32_e32 v149, v77
	v_mov_b32_e32 v150, v134
	s_waitcnt lgkmcnt(0)
	v_mfma_f32_16x16x32_bf16 v[54:57], v[58:61], v[34:37], v[54:57]
	ds_read_b128 v[58:61], v131 offset:43520
	v_mov_b32_e32 v151, v135
	v_mov_b32_e32 v152, v136
	s_waitcnt lgkmcnt(0)
	v_mfma_f32_16x16x32_bf16 v[58:61], v[58:61], v[46:49], 0
	v_mov_b32_e32 v153, v137
	v_mov_b32_e32 v154, v138
	v_mov_b32_e32 v155, v139
	v_mfma_f32_16x16x32_bf16 v[58:61], v[62:65], v[42:45], v[58:61]
	ds_read_b128 v[62:65], v131 offset:43648
	v_mov_b32_e32 v156, v140
	v_mov_b32_e32 v157, v141
	s_waitcnt lgkmcnt(0)
	v_mfma_f32_16x16x32_bf16 v[58:61], v[62:65], v[38:41], v[58:61]
	ds_read_b128 v[62:65], v131 offset:43712
	v_permlane32_swap_b32_e32 v70, v142
	s_waitcnt lgkmcnt(0)
	v_mfma_f32_16x16x32_bf16 v[58:61], v[62:65], v[34:37], v[58:61]
	ds_read_b128 v[62:65], v131 offset:47872
	v_permlane32_swap_b32_e32 v71, v143
	s_waitcnt lgkmcnt(0)
	v_mfma_f32_16x16x32_bf16 v[62:65], v[62:65], v[46:49], 0
	v_permlane32_swap_b32_e32 v72, v144
	v_permlane32_swap_b32_e32 v73, v145
	v_mfma_f32_16x16x32_bf16 v[62:65], v[66:69], v[42:45], v[62:65]
	ds_read_b128 v[66:69], v131 offset:48000
	v_permlane32_swap_b32_e32 v74, v146
	s_waitcnt lgkmcnt(0)
	v_mfma_f32_16x16x32_bf16 v[62:65], v[66:69], v[38:41], v[62:65]
	ds_read_b128 v[66:69], v131 offset:48064
	v_permlane32_swap_b32_e32 v75, v147
	s_waitcnt lgkmcnt(0)
	v_mfma_f32_16x16x32_bf16 v[62:65], v[66:69], v[34:37], v[62:65]
	ds_read_b128 v[66:69], v131 offset:52224
	v_permlane32_swap_b32_e32 v76, v148
	s_waitcnt lgkmcnt(0)
	v_mfma_f32_16x16x32_bf16 v[66:69], v[66:69], v[46:49], 0
	v_permlane32_swap_b32_e32 v77, v149
	v_permlane32_swap_b32_e32 v134, v150
	v_mfma_f32_16x16x32_bf16 v[66:69], v[158:161], v[42:45], v[66:69]
	ds_read_b128 v[158:161], v131 offset:52352
	v_permlane32_swap_b32_e32 v135, v151
	s_waitcnt lgkmcnt(0)
	v_mfma_f32_16x16x32_bf16 v[66:69], v[158:161], v[38:41], v[66:69]
	ds_read_b128 v[158:161], v131 offset:52416
	v_permlane32_swap_b32_e32 v136, v152
	s_waitcnt lgkmcnt(0)
	v_mfma_f32_16x16x32_bf16 v[66:69], v[158:161], v[34:37], v[66:69]
	ds_read_b128 v[158:161], v131 offset:56576
	v_permlane32_swap_b32_e32 v137, v153
	s_waitcnt lgkmcnt(0)
	v_mfma_f32_16x16x32_bf16 v[158:161], v[158:161], v[46:49], 0
	v_permlane32_swap_b32_e32 v138, v154
	v_permlane32_swap_b32_e32 v139, v155
	v_mfma_f32_16x16x32_bf16 v[158:161], v[162:165], v[42:45], v[158:161]
	ds_read_b128 v[162:165], v131 offset:56704
	v_permlane32_swap_b32_e32 v140, v156
	s_waitcnt lgkmcnt(0)
	v_mfma_f32_16x16x32_bf16 v[158:161], v[162:165], v[38:41], v[158:161]
	ds_read_b128 v[162:165], v131 offset:56768
	v_permlane32_swap_b32_e32 v141, v157
	s_waitcnt lgkmcnt(0)
	v_mfma_f32_16x16x32_bf16 v[158:161], v[162:165], v[34:37], v[158:161]
	ds_read_b128 v[162:165], v131 offset:60928
	s_waitcnt lgkmcnt(0)
	v_mfma_f32_16x16x32_bf16 v[162:165], v[162:165], v[46:49], 0
	v_mfma_f32_16x16x32_bf16 v[162:165], v[166:169], v[42:45], v[162:165]
	ds_read_b128 v[166:169], v131 offset:61056
	s_waitcnt lgkmcnt(0)
	v_mfma_f32_16x16x32_bf16 v[162:165], v[166:169], v[38:41], v[162:165]
	ds_read_b128 v[166:169], v131 offset:61120
	s_waitcnt lgkmcnt(0)
	v_mfma_f32_16x16x32_bf16 v[162:165], v[166:169], v[34:37], v[162:165]
	ds_read_b128 v[166:169], v131 offset:65280
	s_waitcnt lgkmcnt(0)
	v_mfma_f32_16x16x32_bf16 v[46:49], v[166:169], v[46:49], 0
	ds_read_b128 v[166:169], v131 offset:65344
	s_waitcnt lgkmcnt(0)
	v_mfma_f32_16x16x32_bf16 v[42:45], v[166:169], v[42:45], v[46:49]
	s_nop 4
	ds_read_b128 v[46:49], v131 offset:65408
	s_waitcnt lgkmcnt(0)
	v_mfma_f32_16x16x32_bf16 v[38:41], v[46:49], v[38:41], v[42:45]
	s_nop 2
	ds_read_b128 v[42:45], v131 offset:65472
	s_waitcnt lgkmcnt(0)
; __device__ __forceinline__ unsigned mono(float f) { const unsigned u = __float_as_uint(f); return (u & 0x80000000u) ? ~u : (u ^ 0x80000000u); }
; __device__ __forceinline__ void topk_phase(LAS unsigned char* lds, const bf16_t* qp, const bf16_t* keys, const float* SU, const float* SV, int* sel_e, float* sel_g, float* sel_su, int G, int b) {
;     ...
;             unsigned lo16[16];
; #pragma unroll
;             for (int mt = 0; mt < 4; ++mt)
; #pragma unroll
;                 for (int r = 0; r < 4; ++r) {
;                     T[p][mt * 4 + r] = (mono(acc[mt][r]) & ~127u) | (unsigned)(127 - (mt * 16 + fq * 4 + r));
;                     lo16[mt * 4 + r] = (mono(acc[mt + 4][r]) & ~127u) | (unsigned)(127 - ((mt + 4) * 16 + fq * 4 + r));
;                 }
;             SN_SORT16(T[p]); SN_SORT16(lo16);
	v_mfma_f32_16x16x32_bf16 v[34:37], v[42:45], v[34:37], v[38:41]
	s_nop 2
	v_ashrrev_i32_e32 v38, 31, v50
	v_bitop3_b32 v38, v50, v38, v132 bitop3:0x1e
	v_and_or_b32 v38, v38, s53, v98
	v_ashrrev_i32_e32 v39, 31, v66
	v_bitop3_b32 v39, v66, v39, v132 bitop3:0x1e
	v_and_or_b32 v39, v39, s53, v99
	v_ashrrev_i32_e32 v40, 31, v51
	v_bitop3_b32 v40, v51, v40, v132 bitop3:0x1e
	v_and_or_b32 v40, v40, s53, v100
	v_ashrrev_i32_e32 v41, 31, v67
	v_bitop3_b32 v41, v67, v41, v132 bitop3:0x1e
	v_and_or_b32 v41, v41, s53, v101
	v_ashrrev_i32_e32 v42, 31, v52
	v_bitop3_b32 v42, v52, v42, v132 bitop3:0x1e
	v_and_or_b32 v42, v42, s53, v102
	v_ashrrev_i32_e32 v43, 31, v68
	v_bitop3_b32 v43, v68, v43, v132 bitop3:0x1e
	v_and_or_b32 v43, v43, s53, v103
	v_ashrrev_i32_e32 v44, 31, v53
	v_bitop3_b32 v44, v53, v44, v132 bitop3:0x1e
	v_and_or_b32 v44, v44, s53, v104
	v_ashrrev_i32_e32 v45, 31, v69
	v_bitop3_b32 v45, v69, v45, v132 bitop3:0x1e
	v_and_or_b32 v45, v45, s53, v105
	v_ashrrev_i32_e32 v46, 31, v54
	v_bitop3_b32 v46, v54, v46, v132 bitop3:0x1e
	v_and_or_b32 v46, v46, s53, v106
	v_ashrrev_i32_e32 v47, 31, v158
	v_bitop3_b32 v47, v158, v47, v132 bitop3:0x1e
	v_and_or_b32 v47, v47, s53, v107
	v_ashrrev_i32_e32 v48, 31, v55
	v_bitop3_b32 v48, v55, v48, v132 bitop3:0x1e
	v_and_or_b32 v48, v48, s53, v108
	v_ashrrev_i32_e32 v49, 31, v159
	v_bitop3_b32 v49, v159, v49, v132 bitop3:0x1e
	v_and_or_b32 v49, v49, s53, v109
	v_ashrrev_i32_e32 v50, 31, v56
	v_bitop3_b32 v50, v56, v50, v132 bitop3:0x1e
	v_and_or_b32 v50, v50, s53, v110
	v_ashrrev_i32_e32 v51, 31, v160
	v_bitop3_b32 v51, v160, v51, v132 bitop3:0x1e
	v_max_u32_e32 v160, v39, v41
	v_ashrrev_i32_e32 v52, 31, v57
	v_bitop3_b32 v52, v57, v52, v132 bitop3:0x1e
	v_min_u32_e32 v39, v39, v41
	v_ashrrev_i32_e32 v53, 31, v161
	v_bitop3_b32 v53, v161, v53, v132 bitop3:0x1e
	v_max_u32_e32 v41, v43, v45
	v_ashrrev_i32_e32 v54, 31, v58
	v_cmp_lt_i32_e32 vcc, -1, v162
	v_bitop3_b32 v54, v58, v54, v132 bitop3:0x1e
	v_min_u32_e32 v43, v43, v45
	v_cndmask_b32_e32 v55, -1, v132, vcc
	v_and_or_b32 v51, v51, s53, v111
	v_and_or_b32 v52, v52, s53, v112
	v_ashrrev_i32_e32 v56, 31, v59
	v_cmp_lt_i32_e32 vcc, -1, v163
	v_bitop3_b32 v56, v59, v56, v132 bitop3:0x1e
	v_and_or_b32 v53, v53, s53, v113
	v_cndmask_b32_e32 v57, -1, v132, vcc
	v_max_u32_e32 v45, v160, v41
	v_min_u32_e32 v41, v160, v41
	v_ashrrev_i32_e32 v58, 31, v60
	v_cmp_lt_i32_e32 vcc, -1, v164
	v_bitop3_b32 v58, v60, v58, v132 bitop3:0x1e
	v_max_u32_e32 v160, v39, v43
	v_cndmask_b32_e32 v59, -1, v132, vcc
	v_min_u32_e32 v39, v39, v43
	v_max_u32_e32 v43, v160, v41
	v_ashrrev_i32_e32 v60, 31, v61
	v_cmp_lt_i32_e32 vcc, -1, v165
	v_bitop3_b32 v60, v61, v60, v132 bitop3:0x1e
	v_min_u32_e32 v41, v160, v41
	v_cndmask_b32_e32 v61, -1, v132, vcc
	v_max_u32_e32 v160, v47, v49
	v_min_u32_e32 v47, v47, v49
	v_ashrrev_i32_e32 v66, 31, v62
	v_bitop3_b32 v62, v62, v66, v132 bitop3:0x1e
	v_max_u32_e32 v49, v51, v53
	v_ashrrev_i32_e32 v66, 31, v34
	v_bitop3_b32 v34, v34, v66, v132 bitop3:0x1e
	v_min_u32_e32 v51, v51, v53
	v_ashrrev_i32_e32 v66, 31, v63
	v_bitop3_b32 v63, v63, v66, v132 bitop3:0x1e
	v_max_u32_e32 v53, v160, v49
	v_ashrrev_i32_e32 v66, 31, v35
	v_bitop3_b32 v35, v35, v66, v132 bitop3:0x1e
	v_min_u32_e32 v49, v160, v49
	v_ashrrev_i32_e32 v66, 31, v64
	v_bitop3_b32 v64, v64, v66, v132 bitop3:0x1e
	v_max_u32_e32 v160, v47, v51
	v_ashrrev_i32_e32 v66, 31, v36
	v_bitop3_b32 v36, v36, v66, v132 bitop3:0x1e
	v_min_u32_e32 v47, v47, v51
	v_ashrrev_i32_e32 v66, 31, v65
	v_cmp_lt_i32_e32 vcc, -1, v37
	v_bitop3_b32 v65, v65, v66, v132 bitop3:0x1e
	v_max_u32_e32 v51, v160, v49
	v_cndmask_b32_e32 v66, -1, v132, vcc
	v_xor_b32_e32 v37, v66, v37
	v_max_u32_e32 v66, v38, v40
	v_min_u32_e32 v38, v38, v40
	v_max_u32_e32 v40, v42, v44
	v_min_u32_e32 v42, v42, v44
	v_max_u32_e32 v44, v66, v40
	v_min_u32_e32 v40, v66, v40
	v_max_u32_e32 v66, v38, v42
	v_min_u32_e32 v38, v38, v42
	v_max_u32_e32 v42, v66, v40
	v_min_u32_e32 v40, v66, v40
	v_max_u32_e32 v66, v46, v48
	v_min_u32_e32 v46, v46, v48
	v_max_u32_e32 v48, v50, v52
	v_min_u32_e32 v50, v50, v52
	v_max_u32_e32 v52, v66, v48
	v_min_u32_e32 v48, v66, v48
	v_max_u32_e32 v66, v46, v50
	v_min_u32_e32 v46, v46, v50
	v_max_u32_e32 v50, v66, v48
	v_min_u32_e32 v48, v66, v48
	v_min_u32_e32 v49, v160, v49
	v_max_u32_e32 v66, v44, v52
	v_min_u32_e32 v44, v44, v52
	v_max_u32_e32 v52, v40, v48
	v_max_u32_e32 v160, v45, v53
	v_min_u32_e32 v45, v45, v53
	v_max_u32_e32 v53, v41, v49
	v_xor_b32_e32 v55, v55, v162
	v_xor_b32_e32 v57, v57, v163
	v_xor_b32_e32 v59, v59, v164
	v_xor_b32_e32 v61, v61, v165
	v_min_u32_e32 v40, v40, v48
	v_max_u32_e32 v48, v52, v44
	v_min_u32_e32 v44, v52, v44
	v_max_u32_e32 v52, v42, v50
	v_min_u32_e32 v42, v42, v50
	v_max_u32_e32 v50, v38, v46
	v_min_u32_e32 v41, v41, v49
	v_max_u32_e32 v49, v53, v45
	v_min_u32_e32 v45, v53, v45
	v_max_u32_e32 v53, v43, v51
	v_min_u32_e32 v43, v43, v51
	v_max_u32_e32 v51, v39, v47
	v_and_or_b32 v54, v54, s53, v114
	v_and_or_b32 v55, v55, s53, v115
	v_and_or_b32 v56, v56, s53, v116
	v_and_or_b32 v57, v57, s53, v117
	v_and_or_b32 v58, v58, s53, v118
	v_and_or_b32 v59, v59, s53, v119
	v_and_or_b32 v60, v60, s53, v120
	v_and_or_b32 v61, v61, s53, v121
	v_min_u32_e32 v38, v38, v46
	v_max_u32_e32 v46, v50, v42
	v_min_u32_e32 v42, v50, v42
	v_min_u32_e32 v39, v39, v47
	v_max_u32_e32 v47, v51, v43
	v_min_u32_e32 v43, v51, v43
	v_max_u32_e32 v50, v52, v48
	v_min_u32_e32 v48, v52, v48
	v_max_u32_e32 v52, v46, v44
	v_min_u32_e32 v44, v46, v44
	v_max_u32_e32 v46, v42, v40
	v_min_u32_e32 v40, v42, v40
	v_max_u32_e32 v42, v54, v56
	v_min_u32_e32 v54, v54, v56
	v_max_u32_e32 v56, v58, v60
; __device__ __forceinline__ void topk_phase(LAS unsigned char* lds, const bf16_t* qp, const bf16_t* keys, const float* SU, const float* SV, int* sel_e, float* sel_g, float* sel_su, int G, int b) {
;     ...
;             SN_SORT16(T[p]); SN_SORT16(lo16);
; #pragma unroll
;             for (int i = 0; i < 16; ++i) T[p][i] = umax_(T[p][i], lo16[15 - i]);
;             SN_BITONIC16(T[p]);
	v_min_u32_e32 v58, v58, v60
	v_max_u32_e32 v51, v53, v49
	v_min_u32_e32 v49, v53, v49
	v_max_u32_e32 v53, v47, v45
	v_min_u32_e32 v45, v47, v45
	v_max_u32_e32 v47, v43, v41
	v_min_u32_e32 v41, v43, v41
	v_max_u32_e32 v43, v55, v57
	v_min_u32_e32 v55, v55, v57
	v_max_u32_e32 v57, v59, v61
	v_min_u32_e32 v59, v59, v61
	v_and_or_b32 v62, v62, s53, v122
	v_and_or_b32 v34, v34, s53, v123
	v_and_or_b32 v63, v63, s53, v124
	v_and_or_b32 v35, v35, s53, v125
	v_and_or_b32 v64, v64, s53, v126
	v_and_or_b32 v36, v36, s53, v127
	v_and_or_b32 v65, v65, s53, v128
	v_and_or_b32 v37, v37, s53, v129
	v_max_u32_e32 v60, v42, v56
	v_min_u32_e32 v42, v42, v56
	v_max_u32_e32 v56, v54, v58
	v_max_u32_e32 v61, v43, v57
	v_min_u32_e32 v43, v43, v57
	v_max_u32_e32 v57, v55, v59
	v_min_u32_e32 v54, v54, v58
	v_max_u32_e32 v58, v56, v42
	v_min_u32_e32 v42, v56, v42
	v_max_u32_e32 v56, v62, v63
	v_min_u32_e32 v62, v62, v63
	v_max_u32_e32 v63, v64, v65
	v_min_u32_e32 v64, v64, v65
	v_min_u32_e32 v55, v55, v59
	v_max_u32_e32 v59, v57, v43
	v_min_u32_e32 v43, v57, v43
	v_max_u32_e32 v57, v34, v35
	v_min_u32_e32 v34, v34, v35
	v_max_u32_e32 v35, v36, v37
	v_min_u32_e32 v36, v36, v37
	v_max_u32_e32 v65, v56, v63
	v_min_u32_e32 v56, v56, v63
	v_max_u32_e32 v63, v62, v64
	v_max_u32_e32 v37, v57, v35
	v_min_u32_e32 v35, v57, v35
	v_max_u32_e32 v57, v34, v36
	v_min_u32_e32 v62, v62, v64
	v_max_u32_e32 v64, v63, v56
	v_min_u32_e32 v56, v63, v56
	v_min_u32_e32 v34, v34, v36
	v_max_u32_e32 v36, v57, v35
	v_min_u32_e32 v35, v57, v35
	v_max_u32_e32 v63, v60, v65
	v_min_u32_e32 v60, v60, v65
	v_max_u32_e32 v65, v42, v56
	v_max_u32_e32 v57, v61, v37
	v_min_u32_e32 v37, v61, v37
	v_max_u32_e32 v61, v43, v35
	v_min_u32_e32 v42, v42, v56
	v_max_u32_e32 v56, v65, v60
	v_min_u32_e32 v60, v65, v60
	v_max_u32_e32 v65, v58, v64
	v_min_u32_e32 v58, v58, v64
	v_max_u32_e32 v64, v54, v62
	v_min_u32_e32 v35, v43, v35
	v_max_u32_e32 v43, v61, v37
	v_min_u32_e32 v37, v61, v37
	v_max_u32_e32 v61, v59, v36
	v_min_u32_e32 v36, v59, v36
	v_max_u32_e32 v59, v55, v34
	v_min_u32_e32 v54, v54, v62
	v_max_u32_e32 v62, v64, v58
	v_min_u32_e32 v34, v55, v34
	v_max_u32_e32 v55, v59, v36
	v_min_u32_e32 v58, v64, v58
	v_max_u32_e32 v64, v65, v56
	v_min_u32_e32 v56, v65, v56
	v_max_u32_e32 v65, v62, v60
	v_min_u32_e32 v60, v62, v60
	v_min_u32_e32 v36, v59, v36
	v_max_u32_e32 v59, v61, v43
	v_min_u32_e32 v43, v61, v43
	v_max_u32_e32 v61, v55, v37
	v_min_u32_e32 v37, v55, v37
	v_max_u32_e32 v62, v58, v42
	v_min_u32_e32 v42, v58, v42
	v_min_u32_e32 v58, v66, v63
	v_max_u32_e32 v67, v44, v60
	v_max_u32_e32 v55, v36, v35
	v_min_u32_e32 v35, v36, v35
	v_min_u32_e32 v36, v160, v57
	v_max_u32_e32 v161, v45, v37
	v_min_u32_e32 v44, v44, v60
	v_max_u32_e32 v60, v67, v58
	v_min_u32_e32 v58, v67, v58
	v_max_u32_e32 v67, v48, v56
	v_min_u32_e32 v48, v48, v56
	v_max_u32_e32 v56, v40, v42
	v_min_u32_e32 v37, v45, v37
	v_max_u32_e32 v45, v161, v36
	v_min_u32_e32 v36, v161, v36
	v_max_u32_e32 v161, v49, v43
	v_min_u32_e32 v43, v49, v43
	v_max_u32_e32 v49, v41, v35
	v_min_u32_e32 v40, v40, v42
	v_max_u32_e32 v42, v56, v48
	v_min_u32_e32 v48, v56, v48
	v_min_u32_e32 v35, v41, v35
	v_max_u32_e32 v41, v49, v43
	v_min_u32_e32 v43, v49, v43
	v_max_u32_e32 v56, v67, v60
	v_min_u32_e32 v60, v67, v60
	v_max_u32_e32 v67, v42, v58
	v_min_u32_e32 v42, v42, v58
	v_max_u32_e32 v58, v48, v44
	v_min_u32_e32 v44, v48, v44
	v_max_u32_e32 v48, v50, v64
	v_min_u32_e32 v50, v50, v64
	v_max_u32_e32 v64, v46, v62
	v_max_u32_e32 v49, v161, v45
	v_min_u32_e32 v45, v161, v45
	v_max_u32_e32 v161, v41, v36
	v_min_u32_e32 v36, v41, v36
	v_max_u32_e32 v41, v43, v37
	v_min_u32_e32 v37, v43, v37
	v_max_u32_e32 v43, v51, v59
	v_min_u32_e32 v51, v51, v59
	v_max_u32_e32 v59, v47, v55
	v_min_u32_e32 v46, v46, v62
	v_max_u32_e32 v62, v64, v50
	v_min_u32_e32 v50, v64, v50
	v_max_u32_e32 v64, v52, v65
	v_min_u32_e32 v52, v52, v65
	v_max_u32_e32 v65, v38, v54
	v_min_u32_e32 v47, v47, v55
	v_max_u32_e32 v55, v59, v51
	v_min_u32_e32 v51, v59, v51
	v_max_u32_e32 v59, v53, v61
	v_min_u32_e32 v53, v53, v61
	v_max_u32_e32 v61, v39, v34
	v_min_u32_e32 v38, v38, v54
	v_max_u32_e32 v54, v65, v52
	v_min_u32_e32 v52, v65, v52
	v_min_u32_e32 v34, v39, v34
	v_max_u32_e32 v39, v61, v53
	v_min_u32_e32 v53, v61, v53
	v_max_u32_e32 v65, v64, v62
	v_min_u32_e32 v62, v64, v62
	v_max_u32_e32 v64, v54, v50
	v_min_u32_e32 v50, v54, v50
	v_max_u32_e32 v54, v52, v46
	v_min_u32_e32 v46, v52, v46
	v_max_u32_e32 v61, v59, v55
	v_min_u32_e32 v55, v59, v55
	v_max_u32_e32 v59, v39, v51
	v_min_u32_e32 v39, v39, v51
	v_max_u32_e32 v51, v53, v47
	v_min_u32_e32 v47, v53, v47
	v_min_u32_e32 v52, v48, v56
	v_min_u32_e32 v68, v65, v60
	v_min_u32_e32 v69, v62, v67
	v_min_u32_e32 v96, v64, v42
	v_min_u32_e32 v97, v50, v58
	v_min_u32_e32 v158, v54, v44
	v_min_u32_e32 v159, v46, v40
	v_min_u32_e32 v53, v43, v49
	v_min_u32_e32 v162, v61, v45
	v_min_u32_e32 v163, v55, v161
	v_min_u32_e32 v164, v59, v36
	v_min_u32_e32 v165, v39, v41
	v_min_u32_e32 v166, v51, v37
	v_min_u32_e32 v167, v47, v35
	v_max3_u32 v34, v66, v63, v34
	v_max3_u32 v48, v48, v56, v167
	v_max3_u32 v35, v52, v47, v35
	v_max3_u32 v47, v65, v60, v166
	v_max3_u32 v37, v68, v51, v37
	v_max3_u32 v51, v62, v67, v165
	v_max3_u32 v39, v69, v39, v41
	v_max3_u32 v41, v64, v42, v164
	v_max3_u32 v36, v96, v59, v36
	v_max3_u32 v42, v50, v58, v163
	v_max3_u32 v50, v97, v55, v161
	v_max3_u32 v44, v54, v44, v162
	v_max3_u32 v45, v158, v61, v45
	v_max3_u32 v40, v46, v40, v53
	v_max3_u32 v43, v159, v43, v49
	v_max3_u32 v38, v38, v160, v57
	v_max_u32_e32 v46, v34, v36
	v_min_u32_e32 v34, v34, v36
	v_max_u32_e32 v36, v48, v42
	v_min_u32_e32 v42, v48, v42
; __device__ __forceinline__ void topk_phase(LAS unsigned char* lds, const bf16_t* qp, const bf16_t* keys, const float* SU, const float* SV, int* sel_e, float* sel_g, float* sel_su, int G, int b) {
;     ...
;             TOPK_XMERGE(T[p], 16); TOPK_XMERGE(T[p], 32);
	v_max_u32_e32 v48, v35, v50
	v_min_u32_e32 v35, v35, v50
	v_max_u32_e32 v49, v47, v44
	v_min_u32_e32 v44, v47, v44
	v_max_u32_e32 v47, v37, v45
	v_min_u32_e32 v37, v37, v45
	v_max_u32_e32 v45, v51, v40
	v_min_u32_e32 v40, v51, v40
	v_max_u32_e32 v50, v39, v43
	v_min_u32_e32 v39, v39, v43
	v_max_u32_e32 v43, v41, v38
	v_min_u32_e32 v38, v41, v38
	v_max_u32_e32 v41, v46, v47
	v_min_u32_e32 v46, v46, v47
	v_max_u32_e32 v47, v36, v45
	v_min_u32_e32 v36, v36, v45
	v_max_u32_e32 v45, v48, v50
	v_min_u32_e32 v48, v48, v50
	v_max_u32_e32 v50, v49, v43
	v_min_u32_e32 v43, v49, v43
	v_max_u32_e32 v49, v34, v37
	v_min_u32_e32 v34, v34, v37
	v_max_u32_e32 v37, v42, v40
	v_min_u32_e32 v40, v42, v40
	v_max_u32_e32 v42, v35, v39
	v_min_u32_e32 v35, v35, v39
	v_max_u32_e32 v39, v44, v38
	v_min_u32_e32 v38, v44, v38
	v_max_u32_e32 v44, v41, v45
	v_min_u32_e32 v41, v41, v45
	v_max_u32_e32 v45, v47, v50
	v_min_u32_e32 v47, v47, v50
	v_max_u32_e32 v50, v46, v48
	v_min_u32_e32 v46, v46, v48
	v_max_u32_e32 v48, v36, v43
	v_min_u32_e32 v36, v36, v43
	v_max_u32_e32 v43, v49, v42
	v_min_u32_e32 v42, v49, v42
	v_max_u32_e32 v49, v37, v39
	v_min_u32_e32 v37, v37, v39
	v_max_u32_e32 v39, v34, v35
	v_min_u32_e32 v34, v34, v35
	v_max_u32_e32 v35, v40, v38
	v_min_u32_e32 v38, v40, v38
	v_max_u32_e32 v40, v44, v45
	v_min_u32_e32 v44, v44, v45
	v_max_u32_e32 v45, v41, v47
	v_min_u32_e32 v41, v41, v47
	v_max_u32_e32 v47, v50, v48
	v_min_u32_e32 v48, v50, v48
	v_max_u32_e32 v50, v46, v36
	v_min_u32_e32 v36, v46, v36
	v_max_u32_e32 v46, v43, v49
	v_min_u32_e32 v43, v43, v49
	v_max_u32_e32 v49, v42, v37
	v_min_u32_e32 v37, v42, v37
	v_max_u32_e32 v42, v39, v35
	v_min_u32_e32 v35, v39, v35
	v_max_u32_e32 v39, v34, v38
	v_min_u32_e32 v34, v34, v38
	v_mov_b32_e32 v38, v40
	v_mov_b32_e32 v51, v44
	v_mov_b32_e32 v52, v45
	v_mov_b32_e32 v53, v41
	v_mov_b32_e32 v54, v47
	v_mov_b32_e32 v55, v48
	v_mov_b32_e32 v56, v50
	v_mov_b32_e32 v57, v36
	v_mov_b32_e32 v58, v46
	v_mov_b32_e32 v59, v43
	v_mov_b32_e32 v60, v49
	v_mov_b32_e32 v61, v37
	v_mov_b32_e32 v62, v42
	v_mov_b32_e32 v63, v35
	v_mov_b32_e32 v64, v39
	v_mov_b32_e32 v65, v34
	v_permlane16_swap_b32_e32 v40, v38
	v_permlane16_swap_b32_e32 v44, v51
	v_permlane16_swap_b32_e32 v45, v52
	v_permlane16_swap_b32_e32 v41, v53
	v_permlane16_swap_b32_e32 v47, v54
	v_permlane16_swap_b32_e32 v48, v55
	v_permlane16_swap_b32_e32 v50, v56
	v_permlane16_swap_b32_e32 v36, v57
	v_permlane16_swap_b32_e32 v46, v58
	v_permlane16_swap_b32_e32 v43, v59
	v_permlane16_swap_b32_e32 v49, v60
	v_permlane16_swap_b32_e32 v37, v61
	v_permlane16_swap_b32_e32 v42, v62
	v_permlane16_swap_b32_e32 v35, v63
	v_permlane16_swap_b32_e32 v39, v64
	v_permlane16_swap_b32_e32 v34, v65
	v_max_u32_e32 v40, v40, v65
	v_max_u32_e32 v44, v44, v64
	v_max_u32_e32 v45, v45, v63
	v_max_u32_e32 v41, v41, v62
	v_max_u32_e32 v47, v47, v61
	v_max_u32_e32 v48, v48, v60
	v_max_u32_e32 v50, v50, v59
	v_max_u32_e32 v36, v36, v58
	v_max_u32_e32 v46, v46, v57
	v_max_u32_e32 v43, v43, v56
	v_max_u32_e32 v49, v49, v55
	v_max_u32_e32 v37, v37, v54
	v_max_u32_e32 v42, v42, v53
	v_max_u32_e32 v35, v35, v52
	v_max_u32_e32 v39, v39, v51
	v_max_u32_e32 v34, v34, v38
	v_max_u32_e32 v38, v40, v46
	v_min_u32_e32 v40, v40, v46
	v_max_u32_e32 v46, v44, v43
	v_min_u32_e32 v43, v44, v43
	v_max_u32_e32 v44, v45, v49
	v_min_u32_e32 v45, v45, v49
	v_max_u32_e32 v49, v41, v37
	v_min_u32_e32 v37, v41, v37
	v_max_u32_e32 v41, v47, v42
	v_min_u32_e32 v42, v47, v42
	v_max_u32_e32 v47, v48, v35
	v_min_u32_e32 v35, v48, v35
	v_max_u32_e32 v48, v50, v39
	v_min_u32_e32 v39, v50, v39
	v_max_u32_e32 v50, v36, v34
	v_min_u32_e32 v34, v36, v34
	v_max_u32_e32 v36, v38, v41
	v_min_u32_e32 v38, v38, v41
	v_max_u32_e32 v41, v46, v47
	v_min_u32_e32 v46, v46, v47
	v_max_u32_e32 v47, v44, v48
	v_min_u32_e32 v44, v44, v48
	v_max_u32_e32 v48, v49, v50
	v_min_u32_e32 v49, v49, v50
	v_max_u32_e32 v50, v40, v42
	v_min_u32_e32 v40, v40, v42
	v_max_u32_e32 v42, v43, v35
	v_min_u32_e32 v35, v43, v35
	v_max_u32_e32 v43, v45, v39
	v_min_u32_e32 v39, v45, v39
	v_max_u32_e32 v45, v37, v34
	v_min_u32_e32 v34, v37, v34
	v_max_u32_e32 v37, v36, v47
	v_min_u32_e32 v47, v36, v47
	v_max_u32_e32 v51, v41, v48
	v_min_u32_e32 v41, v41, v48
	v_max_u32_e32 v48, v38, v44
	v_min_u32_e32 v44, v38, v44
	v_max_u32_e32 v52, v46, v49
	v_min_u32_e32 v46, v46, v49
	v_max_u32_e32 v49, v50, v43
	v_min_u32_e32 v50, v50, v43
	v_max_u32_e32 v53, v42, v45
	v_min_u32_e32 v55, v42, v45
	v_max_u32_e32 v58, v40, v39
	v_min_u32_e32 v59, v40, v39
	v_max_u32_e32 v60, v35, v34
	v_min_u32_e32 v34, v35, v34
	v_max_u32_e32 v36, v37, v51
	v_min_u32_e32 v37, v37, v51
	v_max_u32_e32 v38, v47, v41
	v_min_u32_e32 v39, v47, v41
	v_max_u32_e32 v40, v48, v52
	v_min_u32_e32 v41, v48, v52
	v_max_u32_e32 v42, v44, v46
	v_min_u32_e32 v43, v44, v46
	v_max_u32_e32 v44, v49, v53
	v_min_u32_e32 v45, v49, v53
	v_max_u32_e32 v54, v50, v55
	v_min_u32_e32 v56, v50, v55
	v_max_u32_e32 v57, v58, v60
	v_min_u32_e32 v66, v58, v60
	v_max_u32_e32 v67, v59, v34
	v_min_u32_e32 v68, v59, v34
	v_mov_b32_e32 v69, v36
	v_mov_b32_e32 v158, v37
	v_mov_b32_e32 v159, v38
	v_mov_b32_e32 v160, v39
	v_mov_b32_e32 v161, v40
	v_mov_b32_e32 v162, v41
	v_mov_b32_e32 v163, v42
	v_mov_b32_e32 v97, v43
	v_mov_b32_e32 v53, v44
	v_mov_b32_e32 v52, v45
	v_mov_b32_e32 v51, v54
	v_mov_b32_e32 v50, v56
	v_mov_b32_e32 v49, v57
	v_mov_b32_e32 v48, v66
	v_mov_b32_e32 v47, v67
	v_mov_b32_e32 v46, v68
	v_permlane32_swap_b32_e32 v36, v69
	v_permlane32_swap_b32_e32 v37, v158
	v_permlane32_swap_b32_e32 v38, v159
	v_permlane32_swap_b32_e32 v39, v160
	v_permlane32_swap_b32_e32 v40, v161
	v_permlane32_swap_b32_e32 v41, v162
; __device__ __forceinline__ float unmono(unsigned u) { return __uint_as_float((u & 0x80000000u) ? (u ^ 0x80000000u) : ~u); }
; __device__ __forceinline__ void topk_phase(LAS unsigned char* lds, const bf16_t* qp, const bf16_t* keys, const float* SU, const float* SV, int* sel_e, float* sel_g, float* sel_su, int G, int b) {
;     ...
;         float v1[16], v2[16];
; #pragma unroll
;         for (int i = 0; i < 16; ++i) { v1[i] = unmono(T[0][i] & ~127u); v2[i] = unmono(T[1][i] & ~127u); }
	v_permlane32_swap_b32_e32 v42, v163
	v_permlane32_swap_b32_e32 v43, v97
	v_permlane32_swap_b32_e32 v44, v53
	v_permlane32_swap_b32_e32 v45, v52
	v_permlane32_swap_b32_e32 v54, v51
	v_permlane32_swap_b32_e32 v56, v50
	v_permlane32_swap_b32_e32 v57, v49
	v_permlane32_swap_b32_e32 v66, v48
	v_permlane32_swap_b32_e32 v67, v47
	v_permlane32_swap_b32_e32 v68, v46
	v_max_u32_e32 v59, v70, v157
	v_max_u32_e32 v60, v71, v156
	v_max_u32_e32 v61, v72, v155
	v_max_u32_e32 v62, v73, v154
	v_max_u32_e32 v63, v74, v153
	v_max_u32_e32 v64, v75, v152
	v_max_u32_e32 v65, v76, v151
	v_max_u32_e32 v70, v77, v150
	v_max_u32_e32 v71, v134, v149
	v_max_u32_e32 v72, v135, v148
	v_max_u32_e32 v73, v136, v147
	v_max_u32_e32 v74, v137, v146
	v_max_u32_e32 v75, v138, v145
	v_max_u32_e32 v76, v139, v144
	v_max_u32_e32 v77, v140, v143
	v_max_u32_e32 v96, v141, v142
	v_max_u32_e32 v46, v36, v46
	v_max_u32_e32 v47, v37, v47
	v_max_u32_e32 v48, v38, v48
	v_max_u32_e32 v49, v39, v49
	v_max_u32_e32 v50, v40, v50
	v_max_u32_e32 v51, v41, v51
	v_max_u32_e32 v52, v42, v52
	v_max_u32_e32 v53, v43, v53
	v_max_u32_e32 v97, v44, v97
	v_max_u32_e32 v134, v45, v163
	v_max_u32_e32 v143, v54, v162
	v_max_u32_e32 v149, v56, v161
	v_max_u32_e32 v150, v57, v160
	v_max_u32_e32 v151, v66, v159
	v_max_u32_e32 v152, v67, v158
	v_max_u32_e32 v153, v68, v69
	v_max_u32_e32 v216, v59, v71
	v_min_u32_e32 v224, v59, v71
	v_max_u32_e32 v217, v60, v72
	v_min_u32_e32 v225, v60, v72
	v_max_u32_e32 v218, v61, v73
	v_min_u32_e32 v226, v61, v73
	v_max_u32_e32 v219, v62, v74
	v_min_u32_e32 v227, v62, v74
	v_max_u32_e32 v220, v63, v75
	v_min_u32_e32 v228, v63, v75
	v_max_u32_e32 v221, v64, v76
	v_min_u32_e32 v229, v64, v76
	v_max_u32_e32 v222, v65, v77
	v_min_u32_e32 v230, v65, v77
	v_max_u32_e32 v223, v70, v96
	v_min_u32_e32 v231, v70, v96
	v_max_u32_e32 v232, v216, v220
	v_min_u32_e32 v236, v216, v220
	v_max_u32_e32 v233, v217, v221
	v_min_u32_e32 v237, v217, v221
	v_max_u32_e32 v234, v218, v222
	v_min_u32_e32 v238, v218, v222
	v_max_u32_e32 v235, v219, v223
	v_min_u32_e32 v239, v219, v223
	v_max_u32_e32 v240, v224, v228
	v_min_u32_e32 v246, v224, v228
	v_max_u32_e32 v241, v225, v229
	v_min_u32_e32 v247, v225, v229
	v_max_u32_e32 v244, v226, v230
	v_min_u32_e32 v248, v226, v230
	v_max_u32_e32 v245, v227, v231
	v_min_u32_e32 v249, v227, v231
	v_max_u32_e32 v216, v232, v234
	v_min_u32_e32 v218, v232, v234
	v_max_u32_e32 v217, v233, v235
	v_min_u32_e32 v219, v233, v235
	v_max_u32_e32 v220, v236, v238
	v_min_u32_e32 v222, v236, v238
	v_max_u32_e32 v221, v237, v239
	v_min_u32_e32 v223, v237, v239
	v_max_u32_e32 v224, v240, v244
	v_min_u32_e32 v226, v240, v244
	v_max_u32_e32 v225, v241, v245
	v_min_u32_e32 v227, v241, v245
	v_max_u32_e32 v228, v246, v248
	v_min_u32_e32 v230, v246, v248
	v_max_u32_e32 v229, v247, v249
	v_min_u32_e32 v231, v247, v249
	v_max_u32_e32 v34, v216, v217
	v_min_u32_e32 v35, v216, v217
	v_max_u32_e32 v36, v218, v219
	v_min_u32_e32 v37, v218, v219
	v_max_u32_e32 v54, v220, v221
	v_min_u32_e32 v55, v220, v221
	v_max_u32_e32 v56, v222, v223
	v_min_u32_e32 v57, v222, v223
	v_max_u32_e32 v58, v224, v225
	v_min_u32_e32 v59, v224, v225
	v_max_u32_e32 v60, v226, v227
	v_min_u32_e32 v61, v226, v227
	v_max_u32_e32 v62, v228, v229
	v_min_u32_e32 v63, v228, v229
	v_max_u32_e32 v64, v230, v231
	v_min_u32_e32 v65, v230, v231
	v_max_u32_e32 v216, v46, v97
	v_min_u32_e32 v224, v46, v97
	v_max_u32_e32 v217, v47, v134
	v_min_u32_e32 v225, v47, v134
	v_max_u32_e32 v218, v48, v143
	v_min_u32_e32 v226, v48, v143
	v_max_u32_e32 v219, v49, v149
	v_min_u32_e32 v227, v49, v149
	v_max_u32_e32 v220, v50, v150
	v_min_u32_e32 v228, v50, v150
	v_max_u32_e32 v221, v51, v151
	v_min_u32_e32 v229, v51, v151
	v_max_u32_e32 v222, v52, v152
	v_min_u32_e32 v230, v52, v152
	v_max_u32_e32 v223, v53, v153
	v_min_u32_e32 v231, v53, v153
	v_max_u32_e32 v232, v216, v220
	v_min_u32_e32 v236, v216, v220
	v_max_u32_e32 v233, v217, v221
	v_min_u32_e32 v237, v217, v221
	v_max_u32_e32 v234, v218, v222
	v_min_u32_e32 v238, v218, v222
	v_max_u32_e32 v235, v219, v223
	v_min_u32_e32 v239, v219, v223
	v_max_u32_e32 v240, v224, v228
	v_min_u32_e32 v246, v224, v228
	v_max_u32_e32 v241, v225, v229
	v_min_u32_e32 v247, v225, v229
	v_max_u32_e32 v244, v226, v230
	v_min_u32_e32 v248, v226, v230
	v_max_u32_e32 v245, v227, v231
	v_min_u32_e32 v249, v227, v231
	v_max_u32_e32 v216, v232, v234
	v_min_u32_e32 v218, v232, v234
	v_max_u32_e32 v217, v233, v235
	v_min_u32_e32 v219, v233, v235
	v_max_u32_e32 v220, v236, v238
	v_min_u32_e32 v222, v236, v238
	v_max_u32_e32 v221, v237, v239
	v_min_u32_e32 v223, v237, v239
	v_max_u32_e32 v224, v240, v244
	v_min_u32_e32 v226, v240, v244
	v_max_u32_e32 v225, v241, v245
	v_min_u32_e32 v227, v241, v245
	v_max_u32_e32 v228, v246, v248
	v_min_u32_e32 v230, v246, v248
	v_max_u32_e32 v229, v247, v249
	v_min_u32_e32 v231, v247, v249
	v_max_u32_e32 v38, v216, v217
	v_min_u32_e32 v39, v216, v217
	v_max_u32_e32 v40, v218, v219
	v_min_u32_e32 v41, v218, v219
	v_max_u32_e32 v42, v220, v221
	v_min_u32_e32 v43, v220, v221
	v_max_u32_e32 v44, v222, v223
	v_min_u32_e32 v45, v222, v223
	v_max_u32_e32 v46, v224, v225
	v_min_u32_e32 v47, v224, v225
	v_max_u32_e32 v48, v226, v227
	v_min_u32_e32 v49, v226, v227
	v_max_u32_e32 v50, v228, v229
	v_min_u32_e32 v51, v228, v229
	v_max_u32_e32 v52, v230, v231
	v_min_u32_e32 v53, v230, v231
	v_ashrrev_i32_e32 v216, 31, v34
	v_ashrrev_i32_e32 v217, 31, v35
	v_ashrrev_i32_e32 v218, 31, v36
	v_ashrrev_i32_e32 v219, 31, v37
	v_ashrrev_i32_e32 v220, 31, v54
	v_ashrrev_i32_e32 v221, 31, v55
	v_ashrrev_i32_e32 v222, 31, v56
	v_ashrrev_i32_e32 v223, 31, v57
	v_ashrrev_i32_e32 v224, 31, v58
; __device__ __forceinline__ unsigned mono(float f) { const unsigned u = __float_as_uint(f); return (u & 0x80000000u) ? ~u : (u ^ 0x80000000u); }
; __device__ __forceinline__ float unmono(unsigned u) { return __uint_as_float((u & 0x80000000u) ? (u ^ 0x80000000u) : ~u); }
; __device__ __forceinline__ void topk_phase(LAS unsigned char* lds, const bf16_t* qp, const bf16_t* keys, const float* SU, const float* SV, int* sel_e, float* sel_g, float* sel_su, int G, int b) {
;     ...
;         for (int i = 0; i < 16; ++i) { v1[i] = unmono(T[0][i] & ~127u); v2[i] = unmono(T[1][i] & ~127u); }
;         unsigned ck[16];
; #pragma unroll
;         for (int sidx = 0; sidx < 13; ++sidx) {
;             unsigned keyk[4];
; #pragma unroll
;             for (int k = 0; k < 4; ++k) {
;                 const int c = 4 * sidx + k;
;                 if (c < 50) { const int ci = cand_i(c), cj = cand_j(c); keyk[k] = (mono(v1[ci] + v2[cj]) & ~255u) | (unsigned)(255 - (ci * 16 + cj)); }
;                 else keyk[k] = 0u;
;             }
;             ck[sidx] = fq == 0 ? keyk[0] : fq == 1 ? keyk[1] : fq == 2 ? keyk[2] : keyk[3];
;         }
;         ck[13] = 0u; ck[14] = 0u; ck[15] = 0u;
	v_ashrrev_i32_e32 v225, 31, v59
	v_ashrrev_i32_e32 v226, 31, v60
	v_ashrrev_i32_e32 v227, 31, v61
	v_ashrrev_i32_e32 v228, 31, v62
	v_ashrrev_i32_e32 v229, 31, v63
	v_ashrrev_i32_e32 v230, 31, v64
	v_ashrrev_i32_e32 v231, 31, v65
	v_bitop3_b32 v170, v34, v216, s12 bitop3:0x93
	v_bitop3_b32 v171, v35, v217, s12 bitop3:0x93
	v_bitop3_b32 v172, v36, v218, s12 bitop3:0x93
	v_bitop3_b32 v173, v37, v219, s12 bitop3:0x93
	v_bitop3_b32 v174, v54, v220, s12 bitop3:0x93
	v_bitop3_b32 v175, v55, v221, s12 bitop3:0x93
	v_bitop3_b32 v176, v56, v222, s12 bitop3:0x93
	v_bitop3_b32 v177, v57, v223, s12 bitop3:0x93
	v_bitop3_b32 v178, v58, v224, s12 bitop3:0x93
	v_bitop3_b32 v179, v59, v225, s12 bitop3:0x93
	v_bitop3_b32 v180, v60, v226, s12 bitop3:0x93
	v_bitop3_b32 v181, v61, v227, s12 bitop3:0x93
	v_bitop3_b32 v182, v62, v228, s12 bitop3:0x93
	v_bitop3_b32 v183, v63, v229, s12 bitop3:0x93
	v_bitop3_b32 v184, v64, v230, s12 bitop3:0x93
	v_bitop3_b32 v185, v65, v231, s12 bitop3:0x93
	v_ashrrev_i32_e32 v216, 31, v38
	v_ashrrev_i32_e32 v217, 31, v39
	v_ashrrev_i32_e32 v218, 31, v40
	v_ashrrev_i32_e32 v219, 31, v41
	v_ashrrev_i32_e32 v220, 31, v42
	v_ashrrev_i32_e32 v221, 31, v43
	v_ashrrev_i32_e32 v222, 31, v44
	v_ashrrev_i32_e32 v223, 31, v45
	v_ashrrev_i32_e32 v224, 31, v46
	v_ashrrev_i32_e32 v225, 31, v47
	v_ashrrev_i32_e32 v226, 31, v48
	v_ashrrev_i32_e32 v227, 31, v49
	v_ashrrev_i32_e32 v228, 31, v50
	v_ashrrev_i32_e32 v229, 31, v51
	v_ashrrev_i32_e32 v230, 31, v52
	v_ashrrev_i32_e32 v231, 31, v53
	v_bitop3_b32 v186, v38, v216, s12 bitop3:0x93
	v_bitop3_b32 v187, v39, v217, s12 bitop3:0x93
	v_bitop3_b32 v188, v40, v218, s12 bitop3:0x93
	v_bitop3_b32 v189, v41, v219, s12 bitop3:0x93
	v_bitop3_b32 v190, v42, v220, s12 bitop3:0x93
	v_bitop3_b32 v191, v43, v221, s12 bitop3:0x93
	v_bitop3_b32 v192, v44, v222, s12 bitop3:0x93
	v_bitop3_b32 v193, v45, v223, s12 bitop3:0x93
	v_bitop3_b32 v194, v46, v224, s12 bitop3:0x93
	v_bitop3_b32 v195, v47, v225, s12 bitop3:0x93
	v_bitop3_b32 v196, v48, v226, s12 bitop3:0x93
	v_bitop3_b32 v197, v49, v227, s12 bitop3:0x93
	v_bitop3_b32 v198, v50, v228, s12 bitop3:0x93
	v_bitop3_b32 v199, v51, v229, s12 bitop3:0x93
	v_bitop3_b32 v200, v52, v230, s12 bitop3:0x93
	v_bitop3_b32 v201, v53, v231, s12 bitop3:0x93
	v_cndmask_b32_e64 v250, v186, v187, s[16:17]
	v_cndmask_b32_e64 v250, v250, v188, s[18:19]
	v_cndmask_b32_e64 v250, v250, v189, s[20:21]
	v_cndmask_b32_e64 v251, v190, v191, s[16:17]
	v_cndmask_b32_e64 v251, v251, v192, s[18:19]
	v_cndmask_b32_e64 v251, v251, v193, s[20:21]
	v_cndmask_b32_e64 v252, v194, v195, s[16:17]
	v_cndmask_b32_e64 v252, v252, v196, s[18:19]
	v_cndmask_b32_e64 v252, v252, v197, s[20:21]
	v_cndmask_b32_e64 v253, v198, v199, s[16:17]
	v_cndmask_b32_e64 v253, v253, v200, s[18:19]
	v_cndmask_b32_e64 v253, v253, v201, s[20:21]
	v_add_f32_e32 v254, v170, v250
	v_ashrrev_i32_e32 v255, 31, v254
	v_bitop3_b32 v254, v254, v255, v132 bitop3:0x1e
	v_and_or_b32 v68, v254, s60, v203
	v_add_f32_e32 v254, v170, v251
	v_ashrrev_i32_e32 v255, 31, v254
	v_bitop3_b32 v254, v254, v255, v132 bitop3:0x1e
	v_and_or_b32 v69, v254, s60, v204
	v_add_f32_e32 v254, v170, v252
	v_ashrrev_i32_e32 v255, 31, v254
	v_bitop3_b32 v254, v254, v255, v132 bitop3:0x1e
	v_and_or_b32 v97, v254, s60, v205
	v_add_f32_e32 v254, v170, v253
	v_ashrrev_i32_e32 v255, 31, v254
	v_bitop3_b32 v254, v254, v255, v132 bitop3:0x1e
	v_and_or_b32 v134, v254, s60, v206
	v_add_f32_e32 v254, v171, v250
	v_ashrrev_i32_e32 v255, 31, v254
	v_bitop3_b32 v254, v254, v255, v132 bitop3:0x1e
	v_and_or_b32 v142, v254, s60, v207
	v_add_f32_e32 v254, v171, v251
	v_ashrrev_i32_e32 v255, 31, v254
	v_bitop3_b32 v254, v254, v255, v132 bitop3:0x1e
	v_and_or_b32 v143, v254, s60, v208
	v_add_f32_e32 v254, v172, v250
	v_ashrrev_i32_e32 v255, 31, v254
	v_bitop3_b32 v254, v254, v255, v132 bitop3:0x1e
	v_and_or_b32 v144, v254, s60, v209
	v_cndmask_b32_e64 v232, v172, v173, s[16:17]
	v_cndmask_b32_e64 v232, v232, v173, s[22:23]
	v_cndmask_b32_e64 v233, v190, v186, s[16:17]
	v_cndmask_b32_e64 v233, v233, v187, s[18:19]
	v_cndmask_b32_e64 v233, v233, v188, s[20:21]
	v_add_f32_e32 v254, v232, v233
	v_ashrrev_i32_e32 v255, 31, v254
	v_bitop3_b32 v254, v254, v255, v132 bitop3:0x1e
	v_and_or_b32 v145, v254, s60, v210
	v_cndmask_b32_e64 v234, v173, v174, s[16:17]
	v_cndmask_b32_e64 v234, v234, v174, s[22:23]
	v_cndmask_b32_e64 v235, v189, v186, s[16:17]
	v_cndmask_b32_e64 v235, v235, v187, s[18:19]
	v_cndmask_b32_e64 v235, v235, v188, s[20:21]
	v_add_f32_e32 v254, v234, v235
	v_ashrrev_i32_e32 v255, 31, v254
	v_bitop3_b32 v254, v254, v255, v132 bitop3:0x1e
	v_and_or_b32 v135, v254, s60, v211
	v_cndmask_b32_e64 v236, v175, v176, s[22:23]
	v_cndmask_b32_e64 v237, v186, v187, s[24:25]
	v_add_f32_e32 v254, v236, v237
	v_ashrrev_i32_e32 v255, 31, v254
	v_bitop3_b32 v254, v254, v255, v132 bitop3:0x1e
	v_and_or_b32 v136, v254, s60, v212
	v_cndmask_b32_e64 v238, v177, v178, s[18:19]
	v_cndmask_b32_e64 v238, v238, v179, s[20:21]
	v_cndmask_b32_e64 v239, v186, v187, s[16:17]
	v_add_f32_e32 v254, v238, v239
	v_ashrrev_i32_e32 v255, 31, v254
	v_bitop3_b32 v254, v254, v255, v132 bitop3:0x1e
	v_and_or_b32 v70, v254, s60, v213
	v_cndmask_b32_e64 v240, v180, v181, s[16:17]
	v_cndmask_b32_e64 v240, v240, v182, s[18:19]
	v_cndmask_b32_e64 v240, v240, v183, s[20:21]
	v_add_f32_e32 v254, v240, v186
	v_ashrrev_i32_e32 v255, 31, v254
	v_bitop3_b32 v254, v254, v255, v132 bitop3:0x1e
	v_and_or_b32 v71, v254, s60, v214
	v_cndmask_b32_e64 v241, v184, v185, s[16:17]
	v_add_f32_e32 v254, v241, v186
	v_ashrrev_i32_e32 v255, 31, v254
	v_bitop3_b32 v254, v254, v255, v132 bitop3:0x1e
	v_and_or_b32 v67, v254, s60, v215
; __device__ __forceinline__ void topk_phase(LAS unsigned char* lds, const bf16_t* qp, const bf16_t* keys, const float* SU, const float* SV, int* sel_e, float* sel_g, float* sel_su, int G, int b) {
;     ...
;         ck[13] = 0u; ck[14] = 0u; ck[15] = 0u;
;         SN_SORT16(ck);
;         TOPK_XMERGE(ck, 16); TOPK_XMERGE(ck, 32);
	v_cndmask_b32_e64 v67, v67, 0, s[22:23]
	v_max_u32_e32 v66, v68, v69
	v_min_u32_e32 v68, v68, v69
	v_max_u32_e32 v69, v97, v134
	v_min_u32_e32 v72, v97, v134
	v_max_u32_e32 v73, v66, v69
	v_min_u32_e32 v66, v66, v69
	v_max_u32_e32 v69, v68, v72
	v_min_u32_e32 v68, v68, v72
	v_max_u32_e32 v72, v69, v66
	v_min_u32_e32 v66, v69, v66
	v_max_u32_e32 v69, v142, v143
	v_min_u32_e32 v74, v142, v143
	v_max_u32_e32 v75, v144, v145
	v_min_u32_e32 v76, v144, v145
	v_max_u32_e32 v77, v69, v75
	v_min_u32_e32 v69, v69, v75
	v_max_u32_e32 v75, v74, v76
	v_min_u32_e32 v74, v74, v76
	v_max_u32_e32 v76, v75, v69
	v_min_u32_e32 v69, v75, v69
	v_max_u32_e32 v75, v73, v77
	v_min_u32_e32 v73, v73, v77
	v_max_u32_e32 v77, v66, v69
	v_min_u32_e32 v66, v66, v69
	v_max_u32_e32 v69, v77, v73
	v_min_u32_e32 v73, v77, v73
	v_max_u32_e32 v77, v72, v76
	v_min_u32_e32 v72, v72, v76
	v_max_u32_e32 v76, v68, v74
	v_min_u32_e32 v68, v68, v74
	v_max_u32_e32 v74, v76, v72
	v_min_u32_e32 v72, v76, v72
	v_max_u32_e32 v76, v77, v69
	v_min_u32_e32 v69, v77, v69
	v_max_u32_e32 v77, v74, v73
	v_min_u32_e32 v73, v74, v73
	v_max_u32_e32 v74, v72, v66
	v_min_u32_e32 v66, v72, v66
	v_max_u32_e32 v72, v135, v136
	v_min_u32_e32 v96, v135, v136
	v_max_u32_e32 v97, v70, v71
	v_min_u32_e32 v70, v70, v71
	v_max_u32_e32 v71, v72, v97
	v_min_u32_e32 v72, v72, v97
	v_max_u32_e32 v97, v96, v70
	v_min_u32_e32 v134, v97, v72
	v_max_u32_e32 v135, v71, v67
	v_min_u32_e32 v67, v71, v67
	v_min_u32_e32 v70, v96, v70
	v_max_u32_e32 v71, v134, v67
	v_min_u32_e32 v134, v134, v67
	v_max_u32_e32 v96, v97, v72
	v_med3_u32 v67, v97, v72, v67
	v_max_u32_e32 v72, v70, v134
	v_min_u32_e32 v70, v70, v134
	v_max_u32_e32 v71, v96, v71
	v_max_u32_e32 v96, v75, v135
	v_min_u32_e32 v75, v75, v135
	v_max_u32_e32 v97, v73, v70
	v_min_u32_e32 v70, v73, v70
	v_max_u32_e32 v73, v97, v75
	v_min_u32_e32 v75, v97, v75
	v_max_u32_e32 v97, v69, v67
	v_min_u32_e32 v67, v69, v67
	v_max_u32_e32 v69, v66, v67
	v_min_u32_e32 v66, v66, v67
	v_max_u32_e32 v67, v97, v73
	v_min_u32_e32 v73, v97, v73
	v_max_u32_e32 v97, v69, v75
	v_min_u32_e32 v69, v69, v75
	v_max_u32_e32 v75, v66, v70
	v_min_u32_e32 v66, v66, v70
	v_max_u32_e32 v70, v76, v71
	v_min_u32_e32 v71, v76, v71
	v_max_u32_e32 v76, v74, v71
	v_min_u32_e32 v71, v74, v71
	v_max_u32_e32 v74, v77, v72
	v_min_u32_e32 v72, v77, v72
	v_max_u32_e32 v77, v68, v72
	v_min_u32_e32 v68, v68, v72
	v_max_u32_e32 v72, v74, v76
	v_min_u32_e32 v74, v74, v76
	v_max_u32_e32 v76, v77, v71
	v_min_u32_e32 v71, v77, v71
	v_max_u32_e32 v77, v70, v67
	v_min_u32_e32 v67, v70, v67
	v_max_u32_e32 v70, v72, v73
	v_min_u32_e32 v72, v72, v73
	v_max_u32_e32 v73, v74, v97
	v_min_u32_e32 v74, v74, v97
	v_max_u32_e32 v97, v76, v69
	v_min_u32_e32 v69, v76, v69
	v_max_u32_e32 v76, v71, v75
	v_min_u32_e32 v71, v71, v75
	v_max_u32_e32 v75, v68, v66
	v_min_u32_e32 v66, v68, v66
	v_mov_b32_e32 v68, v96
	v_mov_b32_e32 v134, v77
	v_mov_b32_e32 v135, v67
	v_mov_b32_e32 v136, v70
	v_mov_b32_e32 v137, v72
	v_mov_b32_e32 v138, v73
	v_mov_b32_e32 v139, v74
	v_mov_b32_e32 v140, v97
	v_mov_b32_e32 v141, v69
	v_mov_b32_e32 v142, v76
	v_mov_b32_e32 v143, v71
	v_mov_b32_e32 v144, v75
	v_mov_b32_e32 v145, v66
	v_mov_b32_e32 v146, 0
	v_mov_b32_e32 v147, 0
	v_permlane16_swap_b32_e32 v96, v68
	v_permlane16_swap_b32_e32 v77, v134
	v_permlane16_swap_b32_e32 v67, v135
	v_permlane16_swap_b32_e32 v70, v136
	v_permlane16_swap_b32_e32 v72, v137
	v_permlane16_swap_b32_e32 v73, v138
	v_permlane16_swap_b32_e32 v74, v139
	v_permlane16_swap_b32_e32 v97, v140
	v_permlane16_swap_b32_e32 v69, v141
	v_permlane16_swap_b32_e32 v76, v142
	v_permlane16_swap_b32_e32 v71, v143
	v_permlane16_swap_b32_e32 v75, v144
	v_permlane16_swap_b32_e32 v66, v145
	v_permlane16_swap_b32_e32 v146, v147
; __device__ __forceinline__ void topk_phase(LAS unsigned char* lds, const bf16_t* qp, const bf16_t* keys, const float* SU, const float* SV, int* sel_e, float* sel_g, float* sel_su, int G, int b) {
;     ...
;         TOPK_XMERGE(ck, 16); TOPK_XMERGE(ck, 32);
;         if (fq == 0) {
; #pragma unroll
;             for (int i = 0; i < 16; ++i) { wl[i] = T[0][i]; wl[16 + i] = T[1][i]; }
;         }
	v_max_u32_e32 v96, v96, v147
	v_max_u32_e32 v77, v77, v147
	v_max_u32_e32 v67, v67, v147
	v_max_u32_e32 v70, v70, v145
	v_max_u32_e32 v72, v72, v144
	v_max_u32_e32 v73, v73, v143
	v_max_u32_e32 v74, v74, v142
	v_max_u32_e32 v97, v97, v141
	v_max_u32_e32 v69, v69, v140
	v_max_u32_e32 v76, v76, v139
	v_max_u32_e32 v71, v71, v138
	v_max_u32_e32 v75, v75, v137
	v_max_u32_e32 v66, v66, v136
	v_max_u32_e32 v135, v146, v135
	v_max_u32_e32 v134, v146, v134
	v_max_u32_e32 v68, v146, v68
	v_max_u32_e32 v136, v96, v69
	v_min_u32_e32 v69, v96, v69
	v_max_u32_e32 v96, v77, v76
	v_min_u32_e32 v76, v77, v76
	v_max_u32_e32 v77, v67, v71
	v_min_u32_e32 v67, v67, v71
	v_max_u32_e32 v71, v70, v75
	v_min_u32_e32 v70, v70, v75
	v_max_u32_e32 v75, v72, v66
	v_min_u32_e32 v66, v72, v66
	v_max_u32_e32 v72, v73, v135
	v_min_u32_e32 v73, v73, v135
	v_max_u32_e32 v135, v74, v134
	v_min_u32_e32 v74, v74, v134
	v_max_u32_e32 v134, v97, v68
	v_min_u32_e32 v68, v97, v68
	v_max_u32_e32 v97, v136, v75
	v_min_u32_e32 v75, v136, v75
	v_max_u32_e32 v136, v96, v72
	v_min_u32_e32 v72, v96, v72
	v_max_u32_e32 v96, v77, v135
	v_min_u32_e32 v77, v77, v135
	v_max_u32_e32 v135, v71, v134
	v_min_u32_e32 v71, v71, v134
	v_max_u32_e32 v134, v69, v66
	v_min_u32_e32 v66, v69, v66
	v_max_u32_e32 v69, v76, v73
	v_min_u32_e32 v73, v76, v73
	v_max_u32_e32 v76, v67, v74
	v_min_u32_e32 v67, v67, v74
	v_max_u32_e32 v74, v70, v68
	v_min_u32_e32 v68, v70, v68
	v_max_u32_e32 v70, v97, v96
	v_min_u32_e32 v96, v97, v96
	v_max_u32_e32 v97, v136, v135
	v_min_u32_e32 v135, v136, v135
	v_max_u32_e32 v136, v75, v77
	v_min_u32_e32 v75, v75, v77
	v_max_u32_e32 v77, v72, v71
	v_min_u32_e32 v137, v72, v71
	v_max_u32_e32 v138, v134, v76
	v_min_u32_e32 v134, v134, v76
	v_max_u32_e32 v76, v69, v74
	v_min_u32_e32 v139, v69, v74
	v_max_u32_e32 v140, v66, v67
	v_min_u32_e32 v141, v66, v67
	v_max_u32_e32 v142, v73, v68
	v_min_u32_e32 v143, v73, v68
	v_max_u32_e32 v66, v70, v97
	v_min_u32_e32 v67, v70, v97
	v_max_u32_e32 v68, v96, v135
	v_min_u32_e32 v69, v96, v135
	v_max_u32_e32 v70, v136, v77
	v_min_u32_e32 v71, v136, v77
	v_max_u32_e32 v72, v75, v137
	v_min_u32_e32 v73, v75, v137
	v_max_u32_e32 v74, v138, v76
	v_min_u32_e32 v75, v138, v76
	v_max_u32_e32 v76, v134, v139
	v_min_u32_e32 v77, v134, v139
	v_max_u32_e32 v96, v140, v142
	v_min_u32_e32 v97, v140, v142
	v_max_u32_e32 v134, v141, v143
	v_min_u32_e32 v135, v141, v143
	v_mov_b32_e32 v136, v66
	v_mov_b32_e32 v137, v67
	v_mov_b32_e32 v138, v68
	v_mov_b32_e32 v139, v69
	v_mov_b32_e32 v140, v70
	v_mov_b32_e32 v141, v71
	v_mov_b32_e32 v142, v72
	v_mov_b32_e32 v143, v73
	v_mov_b32_e32 v144, v74
	v_mov_b32_e32 v145, v75
	v_mov_b32_e32 v146, v76
	v_mov_b32_e32 v147, v77
	v_mov_b32_e32 v148, v96
	v_mov_b32_e32 v149, v97
	v_mov_b32_e32 v150, v134
	v_mov_b32_e32 v151, v135
	v_permlane32_swap_b32_e32 v66, v136
	v_permlane32_swap_b32_e32 v67, v137
	v_permlane32_swap_b32_e32 v68, v138
	v_permlane32_swap_b32_e32 v69, v139
	v_permlane32_swap_b32_e32 v70, v140
	v_permlane32_swap_b32_e32 v71, v141
	v_permlane32_swap_b32_e32 v72, v142
	v_permlane32_swap_b32_e32 v73, v143
	v_permlane32_swap_b32_e32 v74, v144
	v_permlane32_swap_b32_e32 v75, v145
	v_permlane32_swap_b32_e32 v76, v146
	v_permlane32_swap_b32_e32 v77, v147
	v_permlane32_swap_b32_e32 v96, v148
	v_permlane32_swap_b32_e32 v97, v149
	v_permlane32_swap_b32_e32 v134, v150
	v_permlane32_swap_b32_e32 v135, v151
	s_and_saveexec_b64 s[0:1], s[40:41]
	s_cbranch_execz .LBB0_739
	ds_write_b128 v83, v[34:37]
	ds_write_b128 v83, v[38:41] offset:64
	ds_write_b128 v83, v[54:57] offset:16
	ds_write_b128 v83, v[42:45] offset:80
	ds_write_b128 v83, v[58:61] offset:32
	ds_write_b128 v83, v[46:49] offset:96
	ds_write_b128 v83, v[62:65] offset:48
	ds_write_b128 v83, v[50:53] offset:112
